# speedup vs baseline: 1.0181x; 1.0181x over previous
.Lc_go:
	s_cmp_eq_u32 s45, 0
	s_cbranch_scc0 .Lc_par1
	ds_read2_b64 v[48:51], v32 offset0:0 offset1:202
	ds_read_b128 v[120:123], v33 offset:0
	ds_read2_b64 v[10:13], v34 offset0:0 offset1:202
	ds_read2_b64 v[52:55], v32 offset0:1 offset1:203
	ds_read2_b64 v[56:59], v32 offset0:2 offset1:204
	ds_read_b128 v[124:127], v33 offset:16
	ds_read2_b64 v[60:63], v32 offset0:3 offset1:205
	ds_read2_b64 v[64:67], v32 offset0:4 offset1:206
	ds_read_b128 v[128:131], v33 offset:32
	ds_read2_b64 v[68:71], v32 offset0:5 offset1:207
	s_mov_b32 s70, 0
	s_mov_b32 s71, 0
	s_waitcnt lgkmcnt(6)
.Lc0_loop:
	v_pk_fma_f16 v6, v2, v120, v121 op_sel:[0,0,0] op_sel_hi:[1,0,0] neg_lo:[1,0,0] neg_hi:[1,0,0]
	v_pk_fma_f16 v7, v3, v120, v121 op_sel:[0,0,0] op_sel_hi:[1,0,0] neg_lo:[1,0,0] neg_hi:[1,0,0]
	v_pk_fma_f16 v8, v4, v120, v121 op_sel:[0,0,0] op_sel_hi:[1,0,0] neg_lo:[1,0,0] neg_hi:[1,0,0]
	v_pk_fma_f16 v9, v5, v120, v121 op_sel:[0,0,0] op_sel_hi:[1,0,0] neg_lo:[1,0,0] neg_hi:[1,0,0]
	v_mfma_f32_16x16x32_f16 v[18:21], v[10:13], v[2:5], 0
	ds_read2_b64 v[72:75], v32 offset0:6 offset1:208
	ds_read_b128 v[132:135], v33 offset:48
	ds_read_b32 v37, v36 offset:4
	ds_read_b32 v38, v36 offset:68
	v_pk_fma_f16 v2, v48, v6, v2
	v_pk_fma_f16 v3, v49, v7, v3
	v_pk_fma_f16 v4, v50, v8, v4
	v_pk_fma_f16 v5, v51, v9, v5
	v_cndmask_b32_e64 v29, v29, v25, s[66:67]
	v_cvt_pk_f16_f32 v30, v26, v27
	v_cvt_pk_f16_f32 v31, v28, v29
	ds_write_b16 v39, v30 offset:0
	ds_write_b16_d16_hi v39, v30 offset:64
	ds_write_b16 v39, v31 offset:128
	ds_write_b16_d16_hi v39, v31 offset:192
	s_mov_b64 exec, 1
	ds_add_u32 v36, v44 offset:124
	s_mov_b64 exec, -1
	v_pk_fma_f16 v6, v2, v122, v123 op_sel:[0,0,0] op_sel_hi:[1,0,0] neg_lo:[1,0,0] neg_hi:[1,0,0]
	v_pk_fma_f16 v7, v3, v122, v123 op_sel:[0,0,0] op_sel_hi:[1,0,0] neg_lo:[1,0,0] neg_hi:[1,0,0]
	v_pk_fma_f16 v8, v4, v122, v123 op_sel:[0,0,0] op_sel_hi:[1,0,0] neg_lo:[1,0,0] neg_hi:[1,0,0]
	v_pk_fma_f16 v9, v5, v122, v123 op_sel:[0,0,0] op_sel_hi:[1,0,0] neg_lo:[1,0,0] neg_hi:[1,0,0]
	v_mfma_f32_16x16x32_f16 v[22:25], v[10:13], v[2:5], 0
	ds_read2_b64 v[76:79], v32 offset0:7 offset1:209
	s_waitcnt lgkmcnt(13)
	v_pk_fma_f16 v2, v52, v6, v2
	v_pk_fma_f16 v3, v53, v7, v3
	v_pk_fma_f16 v4, v54, v8, v4
	v_pk_fma_f16 v5, v55, v9, v5
	v_cndmask_b32_e64 v26, v26, v18, s[60:61]
	v_pk_fma_f16 v6, v2, v124, v125 op_sel:[0,0,0] op_sel_hi:[1,0,0] neg_lo:[1,0,0] neg_hi:[1,0,0]
	v_pk_fma_f16 v7, v3, v124, v125 op_sel:[0,0,0] op_sel_hi:[1,0,0] neg_lo:[1,0,0] neg_hi:[1,0,0]
	v_pk_fma_f16 v8, v4, v124, v125 op_sel:[0,0,0] op_sel_hi:[1,0,0] neg_lo:[1,0,0] neg_hi:[1,0,0]
	v_pk_fma_f16 v9, v5, v124, v125 op_sel:[0,0,0] op_sel_hi:[1,0,0] neg_lo:[1,0,0] neg_hi:[1,0,0]
	v_mfma_f32_16x16x32_f16 v[18:21], v[10:13], v[2:5], 0
	ds_read2_b64 v[80:83], v32 offset0:8 offset1:210
	ds_read_b128 v[136:139], v33 offset:64
	v_pk_fma_f16 v2, v56, v6, v2
	v_pk_fma_f16 v3, v57, v7, v3
	v_pk_fma_f16 v4, v58, v8, v4
	v_pk_fma_f16 v5, v59, v9, v5
	v_cndmask_b32_e64 v27, v27, v23, s[60:61]
	v_pk_fma_f16 v6, v2, v126, v127 op_sel:[0,0,0] op_sel_hi:[1,0,0] neg_lo:[1,0,0] neg_hi:[1,0,0]
	v_pk_fma_f16 v7, v3, v126, v127 op_sel:[0,0,0] op_sel_hi:[1,0,0] neg_lo:[1,0,0] neg_hi:[1,0,0]
	v_pk_fma_f16 v8, v4, v126, v127 op_sel:[0,0,0] op_sel_hi:[1,0,0] neg_lo:[1,0,0] neg_hi:[1,0,0]
	v_pk_fma_f16 v9, v5, v126, v127 op_sel:[0,0,0] op_sel_hi:[1,0,0] neg_lo:[1,0,0] neg_hi:[1,0,0]
	v_mfma_f32_16x16x32_f16 v[22:25], v[10:13], v[2:5], 0
	ds_read2_b64 v[84:87], v32 offset0:9 offset1:211
	s_waitcnt lgkmcnt(13)
	v_pk_fma_f16 v2, v60, v6, v2
	v_pk_fma_f16 v3, v61, v7, v3
	v_pk_fma_f16 v4, v62, v8, v4
	v_pk_fma_f16 v5, v63, v9, v5
	v_cndmask_b32_e64 v28, v28, v20, s[60:61]
	v_pk_fma_f16 v6, v2, v128, v129 op_sel:[0,0,0] op_sel_hi:[1,0,0] neg_lo:[1,0,0] neg_hi:[1,0,0]
	v_pk_fma_f16 v7, v3, v128, v129 op_sel:[0,0,0] op_sel_hi:[1,0,0] neg_lo:[1,0,0] neg_hi:[1,0,0]
	v_pk_fma_f16 v8, v4, v128, v129 op_sel:[0,0,0] op_sel_hi:[1,0,0] neg_lo:[1,0,0] neg_hi:[1,0,0]
	v_pk_fma_f16 v9, v5, v128, v129 op_sel:[0,0,0] op_sel_hi:[1,0,0] neg_lo:[1,0,0] neg_hi:[1,0,0]
	v_mfma_f32_16x16x32_f16 v[18:21], v[10:13], v[2:5], 0
	ds_read2_b64 v[88:91], v32 offset0:10 offset1:212
	ds_read_b128 v[140:143], v33 offset:80
	v_pk_fma_f16 v2, v64, v6, v2
	v_pk_fma_f16 v3, v65, v7, v3
	v_pk_fma_f16 v4, v66, v8, v4
	v_pk_fma_f16 v5, v67, v9, v5
	v_cndmask_b32_e64 v29, v29, v25, s[60:61]
	v_pk_fma_f16 v6, v2, v130, v131 op_sel:[0,0,0] op_sel_hi:[1,0,0] neg_lo:[1,0,0] neg_hi:[1,0,0]
	v_pk_fma_f16 v7, v3, v130, v131 op_sel:[0,0,0] op_sel_hi:[1,0,0] neg_lo:[1,0,0] neg_hi:[1,0,0]
	v_pk_fma_f16 v8, v4, v130, v131 op_sel:[0,0,0] op_sel_hi:[1,0,0] neg_lo:[1,0,0] neg_hi:[1,0,0]
	v_pk_fma_f16 v9, v5, v130, v131 op_sel:[0,0,0] op_sel_hi:[1,0,0] neg_lo:[1,0,0] neg_hi:[1,0,0]
	v_mfma_f32_16x16x32_f16 v[22:25], v[10:13], v[2:5], 0
	ds_read2_b64 v[92:95], v32 offset0:11 offset1:213
	s_waitcnt lgkmcnt(6)
	v_pk_fma_f16 v2, v68, v6, v2
	v_pk_fma_f16 v3, v69, v7, v3
	v_pk_fma_f16 v4, v70, v8, v4
	v_pk_fma_f16 v5, v71, v9, v5
	v_cndmask_b32_e64 v26, v26, v18, s[62:63]
	v_pk_fma_f16 v6, v2, v132, v133 op_sel:[0,0,0] op_sel_hi:[1,0,0] neg_lo:[1,0,0] neg_hi:[1,0,0]
	v_pk_fma_f16 v7, v3, v132, v133 op_sel:[0,0,0] op_sel_hi:[1,0,0] neg_lo:[1,0,0] neg_hi:[1,0,0]
	v_pk_fma_f16 v8, v4, v132, v133 op_sel:[0,0,0] op_sel_hi:[1,0,0] neg_lo:[1,0,0] neg_hi:[1,0,0]
	v_pk_fma_f16 v9, v5, v132, v133 op_sel:[0,0,0] op_sel_hi:[1,0,0] neg_lo:[1,0,0] neg_hi:[1,0,0]
	v_mfma_f32_16x16x32_f16 v[18:21], v[10:13], v[2:5], 0
	ds_read2_b64 v[96:99], v32 offset0:12 offset1:214
	ds_read_b128 v[144:147], v33 offset:96
	v_pk_fma_f16 v2, v72, v6, v2
	v_pk_fma_f16 v3, v73, v7, v3
	v_pk_fma_f16 v4, v74, v8, v4
	v_pk_fma_f16 v5, v75, v9, v5
	v_cndmask_b32_e64 v27, v27, v23, s[62:63]
	v_pk_fma_f16 v6, v2, v134, v135 op_sel:[0,0,0] op_sel_hi:[1,0,0] neg_lo:[1,0,0] neg_hi:[1,0,0]
	v_pk_fma_f16 v7, v3, v134, v135 op_sel:[0,0,0] op_sel_hi:[1,0,0] neg_lo:[1,0,0] neg_hi:[1,0,0]
	v_pk_fma_f16 v8, v4, v134, v135 op_sel:[0,0,0] op_sel_hi:[1,0,0] neg_lo:[1,0,0] neg_hi:[1,0,0]
	v_pk_fma_f16 v9, v5, v134, v135 op_sel:[0,0,0] op_sel_hi:[1,0,0] neg_lo:[1,0,0] neg_hi:[1,0,0]
	v_mfma_f32_16x16x32_f16 v[22:25], v[10:13], v[2:5], 0
	ds_read2_b64 v[100:103], v32 offset0:13 offset1:215
	s_waitcnt lgkmcnt(6)
	v_pk_fma_f16 v2, v76, v6, v2
	v_pk_fma_f16 v3, v77, v7, v3
	v_pk_fma_f16 v4, v78, v8, v4
	v_pk_fma_f16 v5, v79, v9, v5
	v_cndmask_b32_e64 v28, v28, v20, s[62:63]
	v_pk_fma_f16 v6, v2, v136, v137 op_sel:[0,0,0] op_sel_hi:[1,0,0] neg_lo:[1,0,0] neg_hi:[1,0,0]
	v_pk_fma_f16 v7, v3, v136, v137 op_sel:[0,0,0] op_sel_hi:[1,0,0] neg_lo:[1,0,0] neg_hi:[1,0,0]
	v_pk_fma_f16 v8, v4, v136, v137 op_sel:[0,0,0] op_sel_hi:[1,0,0] neg_lo:[1,0,0] neg_hi:[1,0,0]
	v_pk_fma_f16 v9, v5, v136, v137 op_sel:[0,0,0] op_sel_hi:[1,0,0] neg_lo:[1,0,0] neg_hi:[1,0,0]
	v_mfma_f32_16x16x32_f16 v[18:21], v[10:13], v[2:5], 0
	ds_read2_b64 v[104:107], v32 offset0:14 offset1:216
	ds_read_b128 v[148:151], v33 offset:112
	v_pk_fma_f16 v2, v80, v6, v2
	v_pk_fma_f16 v3, v81, v7, v3
	v_pk_fma_f16 v4, v82, v8, v4
	v_pk_fma_f16 v5, v83, v9, v5
	v_cndmask_b32_e64 v29, v29, v25, s[62:63]
	v_readfirstlane_b32 s4, v37
	v_readfirstlane_b32 s5, v38
	s_and_b32 s4, s4, s5
	s_cbranch_scc0 .Lc0_slow0
.Lc0_back0:
	v_pk_fma_f16 v6, v2, v138, v139 op_sel:[0,0,0] op_sel_hi:[1,0,0] neg_lo:[1,0,0] neg_hi:[1,0,0]
	v_pk_fma_f16 v7, v3, v138, v139 op_sel:[0,0,0] op_sel_hi:[1,0,0] neg_lo:[1,0,0] neg_hi:[1,0,0]
	v_pk_fma_f16 v8, v4, v138, v139 op_sel:[0,0,0] op_sel_hi:[1,0,0] neg_lo:[1,0,0] neg_hi:[1,0,0]
	v_pk_fma_f16 v9, v5, v138, v139 op_sel:[0,0,0] op_sel_hi:[1,0,0] neg_lo:[1,0,0] neg_hi:[1,0,0]
	v_mfma_f32_16x16x32_f16 v[22:25], v[10:13], v[2:5], 0
	ds_read2_b64 v[108:111], v32 offset0:15 offset1:217
	s_waitcnt lgkmcnt(6)
	v_pk_fma_f16 v2, v84, v6, v2
	v_pk_fma_f16 v3, v85, v7, v3
	v_pk_fma_f16 v4, v86, v8, v4
	v_pk_fma_f16 v5, v87, v9, v5
	v_cndmask_b32_e64 v26, v26, v18, s[64:65]
	v_pk_fma_f16 v6, v2, v140, v141 op_sel:[0,0,0] op_sel_hi:[1,0,0] neg_lo:[1,0,0] neg_hi:[1,0,0]
	v_pk_fma_f16 v7, v3, v140, v141 op_sel:[0,0,0] op_sel_hi:[1,0,0] neg_lo:[1,0,0] neg_hi:[1,0,0]
	v_pk_fma_f16 v8, v4, v140, v141 op_sel:[0,0,0] op_sel_hi:[1,0,0] neg_lo:[1,0,0] neg_hi:[1,0,0]
	v_pk_fma_f16 v9, v5, v140, v141 op_sel:[0,0,0] op_sel_hi:[1,0,0] neg_lo:[1,0,0] neg_hi:[1,0,0]
	v_mfma_f32_16x16x32_f16 v[18:21], v[10:13], v[2:5], 0
	ds_read2_b64 v[48:51], v32 offset0:16 offset1:218
	ds_read_b128 v[120:123], v33 offset:128
	ds_read2_b64 v[14:17], v34 offset0:16 offset1:218
	v_pk_fma_f16 v2, v88, v6, v2
	v_pk_fma_f16 v3, v89, v7, v3
	v_pk_fma_f16 v4, v90, v8, v4
	v_pk_fma_f16 v5, v91, v9, v5
	v_cndmask_b32_e64 v27, v27, v23, s[64:65]
	v_pk_fma_f16 v6, v2, v142, v143 op_sel:[0,0,0] op_sel_hi:[1,0,0] neg_lo:[1,0,0] neg_hi:[1,0,0]
	v_pk_fma_f16 v7, v3, v142, v143 op_sel:[0,0,0] op_sel_hi:[1,0,0] neg_lo:[1,0,0] neg_hi:[1,0,0]
	v_pk_fma_f16 v8, v4, v142, v143 op_sel:[0,0,0] op_sel_hi:[1,0,0] neg_lo:[1,0,0] neg_hi:[1,0,0]
	v_pk_fma_f16 v9, v5, v142, v143 op_sel:[0,0,0] op_sel_hi:[1,0,0] neg_lo:[1,0,0] neg_hi:[1,0,0]
	v_mfma_f32_16x16x32_f16 v[22:25], v[10:13], v[2:5], 0
	ds_read2_b64 v[52:55], v32 offset0:17 offset1:219
	s_waitcnt lgkmcnt(7)
	v_pk_fma_f16 v2, v92, v6, v2
	v_pk_fma_f16 v3, v93, v7, v3
	v_pk_fma_f16 v4, v94, v8, v4
	v_pk_fma_f16 v5, v95, v9, v5
	v_cndmask_b32_e64 v28, v28, v20, s[64:65]
	v_pk_fma_f16 v6, v2, v144, v145 op_sel:[0,0,0] op_sel_hi:[1,0,0] neg_lo:[1,0,0] neg_hi:[1,0,0]
	v_pk_fma_f16 v7, v3, v144, v145 op_sel:[0,0,0] op_sel_hi:[1,0,0] neg_lo:[1,0,0] neg_hi:[1,0,0]
	v_pk_fma_f16 v8, v4, v144, v145 op_sel:[0,0,0] op_sel_hi:[1,0,0] neg_lo:[1,0,0] neg_hi:[1,0,0]
	v_pk_fma_f16 v9, v5, v144, v145 op_sel:[0,0,0] op_sel_hi:[1,0,0] neg_lo:[1,0,0] neg_hi:[1,0,0]
	v_mfma_f32_16x16x32_f16 v[18:21], v[10:13], v[2:5], 0
	ds_read2_b64 v[56:59], v32 offset0:18 offset1:220
	ds_read_b128 v[124:127], v33 offset:144
	v_pk_fma_f16 v2, v96, v6, v2
	v_pk_fma_f16 v3, v97, v7, v3
	v_pk_fma_f16 v4, v98, v8, v4
	v_pk_fma_f16 v5, v99, v9, v5
	v_cndmask_b32_e64 v29, v29, v25, s[64:65]
	v_pk_fma_f16 v6, v2, v146, v147 op_sel:[0,0,0] op_sel_hi:[1,0,0] neg_lo:[1,0,0] neg_hi:[1,0,0]
	v_pk_fma_f16 v7, v3, v146, v147 op_sel:[0,0,0] op_sel_hi:[1,0,0] neg_lo:[1,0,0] neg_hi:[1,0,0]
	v_pk_fma_f16 v8, v4, v146, v147 op_sel:[0,0,0] op_sel_hi:[1,0,0] neg_lo:[1,0,0] neg_hi:[1,0,0]
	v_pk_fma_f16 v9, v5, v146, v147 op_sel:[0,0,0] op_sel_hi:[1,0,0] neg_lo:[1,0,0] neg_hi:[1,0,0]
	v_mfma_f32_16x16x32_f16 v[22:25], v[10:13], v[2:5], 0
	ds_read2_b64 v[60:63], v32 offset0:19 offset1:221
	s_waitcnt lgkmcnt(7)
	v_pk_fma_f16 v2, v100, v6, v2
	v_pk_fma_f16 v3, v101, v7, v3
	v_pk_fma_f16 v4, v102, v8, v4
	v_pk_fma_f16 v5, v103, v9, v5
	v_cndmask_b32_e64 v26, v26, v18, s[66:67]
	v_pk_fma_f16 v6, v2, v148, v149 op_sel:[0,0,0] op_sel_hi:[1,0,0] neg_lo:[1,0,0] neg_hi:[1,0,0]
	v_pk_fma_f16 v7, v3, v148, v149 op_sel:[0,0,0] op_sel_hi:[1,0,0] neg_lo:[1,0,0] neg_hi:[1,0,0]
	v_pk_fma_f16 v8, v4, v148, v149 op_sel:[0,0,0] op_sel_hi:[1,0,0] neg_lo:[1,0,0] neg_hi:[1,0,0]
	v_pk_fma_f16 v9, v5, v148, v149 op_sel:[0,0,0] op_sel_hi:[1,0,0] neg_lo:[1,0,0] neg_hi:[1,0,0]
	v_mfma_f32_16x16x32_f16 v[18:21], v[10:13], v[2:5], 0
	ds_read2_b64 v[64:67], v32 offset0:20 offset1:222
	ds_read_b128 v[128:131], v33 offset:160
	v_pk_fma_f16 v2, v104, v6, v2
	v_pk_fma_f16 v3, v105, v7, v3
	v_pk_fma_f16 v4, v106, v8, v4
	v_pk_fma_f16 v5, v107, v9, v5
	v_cndmask_b32_e64 v27, v27, v23, s[66:67]
	v_pk_fma_f16 v6, v2, v150, v151 op_sel:[0,0,0] op_sel_hi:[1,0,0] neg_lo:[1,0,0] neg_hi:[1,0,0]
	v_pk_fma_f16 v7, v3, v150, v151 op_sel:[0,0,0] op_sel_hi:[1,0,0] neg_lo:[1,0,0] neg_hi:[1,0,0]
	v_pk_fma_f16 v8, v4, v150, v151 op_sel:[0,0,0] op_sel_hi:[1,0,0] neg_lo:[1,0,0] neg_hi:[1,0,0]
	v_pk_fma_f16 v9, v5, v150, v151 op_sel:[0,0,0] op_sel_hi:[1,0,0] neg_lo:[1,0,0] neg_hi:[1,0,0]
	v_mfma_f32_16x16x32_f16 v[22:25], v[10:13], v[2:5], 0
	ds_read2_b64 v[68:71], v32 offset0:21 offset1:223
	s_waitcnt lgkmcnt(6)
	v_pk_fma_f16 v2, v108, v6, v2
	v_pk_fma_f16 v3, v109, v7, v3
	v_pk_fma_f16 v4, v110, v8, v4
	v_pk_fma_f16 v5, v111, v9, v5
	v_cndmask_b32_e64 v28, v28, v20, s[66:67]
.Lc0_next0:
	v_pk_fma_f16 v6, v2, v120, v121 op_sel:[0,0,0] op_sel_hi:[1,0,0] neg_lo:[1,0,0] neg_hi:[1,0,0]
	v_pk_fma_f16 v7, v3, v120, v121 op_sel:[0,0,0] op_sel_hi:[1,0,0] neg_lo:[1,0,0] neg_hi:[1,0,0]
	v_pk_fma_f16 v8, v4, v120, v121 op_sel:[0,0,0] op_sel_hi:[1,0,0] neg_lo:[1,0,0] neg_hi:[1,0,0]
	v_pk_fma_f16 v9, v5, v120, v121 op_sel:[0,0,0] op_sel_hi:[1,0,0] neg_lo:[1,0,0] neg_hi:[1,0,0]
	v_mfma_f32_16x16x32_f16 v[18:21], v[14:17], v[2:5], 0
	ds_read2_b64 v[72:75], v32 offset0:22 offset1:224
	ds_read_b128 v[132:135], v33 offset:176
	ds_read_b32 v37, v36 offset:8
	ds_read_b32 v38, v36 offset:72
	v_pk_fma_f16 v2, v48, v6, v2
	v_pk_fma_f16 v3, v49, v7, v3
	v_pk_fma_f16 v4, v50, v8, v4
	v_pk_fma_f16 v5, v51, v9, v5
	v_cndmask_b32_e64 v29, v29, v25, s[66:67]
	v_cvt_pk_f16_f32 v30, v26, v27
	v_cvt_pk_f16_f32 v31, v28, v29
	ds_write_b16 v39, v30 offset:2048
	ds_write_b16_d16_hi v39, v30 offset:2112
	ds_write_b16 v39, v31 offset:2176
	ds_write_b16_d16_hi v39, v31 offset:2240
	s_mov_b64 exec, 1
	ds_add_u32 v36, v44 offset:128
	s_mov_b64 exec, -1
	v_pk_fma_f16 v6, v2, v122, v123 op_sel:[0,0,0] op_sel_hi:[1,0,0] neg_lo:[1,0,0] neg_hi:[1,0,0]
	v_pk_fma_f16 v7, v3, v122, v123 op_sel:[0,0,0] op_sel_hi:[1,0,0] neg_lo:[1,0,0] neg_hi:[1,0,0]
	v_pk_fma_f16 v8, v4, v122, v123 op_sel:[0,0,0] op_sel_hi:[1,0,0] neg_lo:[1,0,0] neg_hi:[1,0,0]
	v_pk_fma_f16 v9, v5, v122, v123 op_sel:[0,0,0] op_sel_hi:[1,0,0] neg_lo:[1,0,0] neg_hi:[1,0,0]
	v_mfma_f32_16x16x32_f16 v[22:25], v[14:17], v[2:5], 0
	ds_read2_b64 v[76:79], v32 offset0:23 offset1:225
	s_waitcnt lgkmcnt(13)
	v_pk_fma_f16 v2, v52, v6, v2
	v_pk_fma_f16 v3, v53, v7, v3
	v_pk_fma_f16 v4, v54, v8, v4
	v_pk_fma_f16 v5, v55, v9, v5
	v_cndmask_b32_e64 v26, v26, v18, s[60:61]
	v_pk_fma_f16 v6, v2, v124, v125 op_sel:[0,0,0] op_sel_hi:[1,0,0] neg_lo:[1,0,0] neg_hi:[1,0,0]
	v_pk_fma_f16 v7, v3, v124, v125 op_sel:[0,0,0] op_sel_hi:[1,0,0] neg_lo:[1,0,0] neg_hi:[1,0,0]
	v_pk_fma_f16 v8, v4, v124, v125 op_sel:[0,0,0] op_sel_hi:[1,0,0] neg_lo:[1,0,0] neg_hi:[1,0,0]
	v_pk_fma_f16 v9, v5, v124, v125 op_sel:[0,0,0] op_sel_hi:[1,0,0] neg_lo:[1,0,0] neg_hi:[1,0,0]
	v_mfma_f32_16x16x32_f16 v[18:21], v[14:17], v[2:5], 0
	ds_read2_b64 v[80:83], v32 offset0:24 offset1:226
	ds_read_b128 v[136:139], v33 offset:192
	v_pk_fma_f16 v2, v56, v6, v2
	v_pk_fma_f16 v3, v57, v7, v3
	v_pk_fma_f16 v4, v58, v8, v4
	v_pk_fma_f16 v5, v59, v9, v5
	v_cndmask_b32_e64 v27, v27, v23, s[60:61]
	v_pk_fma_f16 v6, v2, v126, v127 op_sel:[0,0,0] op_sel_hi:[1,0,0] neg_lo:[1,0,0] neg_hi:[1,0,0]
	v_pk_fma_f16 v7, v3, v126, v127 op_sel:[0,0,0] op_sel_hi:[1,0,0] neg_lo:[1,0,0] neg_hi:[1,0,0]
	v_pk_fma_f16 v8, v4, v126, v127 op_sel:[0,0,0] op_sel_hi:[1,0,0] neg_lo:[1,0,0] neg_hi:[1,0,0]
	v_pk_fma_f16 v9, v5, v126, v127 op_sel:[0,0,0] op_sel_hi:[1,0,0] neg_lo:[1,0,0] neg_hi:[1,0,0]
	v_mfma_f32_16x16x32_f16 v[22:25], v[14:17], v[2:5], 0
	ds_read2_b64 v[84:87], v32 offset0:25 offset1:227
	s_waitcnt lgkmcnt(13)
	v_pk_fma_f16 v2, v60, v6, v2
	v_pk_fma_f16 v3, v61, v7, v3
	v_pk_fma_f16 v4, v62, v8, v4
	v_pk_fma_f16 v5, v63, v9, v5
	v_cndmask_b32_e64 v28, v28, v20, s[60:61]
	v_pk_fma_f16 v6, v2, v128, v129 op_sel:[0,0,0] op_sel_hi:[1,0,0] neg_lo:[1,0,0] neg_hi:[1,0,0]
	v_pk_fma_f16 v7, v3, v128, v129 op_sel:[0,0,0] op_sel_hi:[1,0,0] neg_lo:[1,0,0] neg_hi:[1,0,0]
	v_pk_fma_f16 v8, v4, v128, v129 op_sel:[0,0,0] op_sel_hi:[1,0,0] neg_lo:[1,0,0] neg_hi:[1,0,0]
	v_pk_fma_f16 v9, v5, v128, v129 op_sel:[0,0,0] op_sel_hi:[1,0,0] neg_lo:[1,0,0] neg_hi:[1,0,0]
	v_mfma_f32_16x16x32_f16 v[18:21], v[14:17], v[2:5], 0
	ds_read2_b64 v[88:91], v32 offset0:26 offset1:228
	ds_read_b128 v[140:143], v33 offset:208
	v_pk_fma_f16 v2, v64, v6, v2
	v_pk_fma_f16 v3, v65, v7, v3
	v_pk_fma_f16 v4, v66, v8, v4
	v_pk_fma_f16 v5, v67, v9, v5
	v_cndmask_b32_e64 v29, v29, v25, s[60:61]
	v_pk_fma_f16 v6, v2, v130, v131 op_sel:[0,0,0] op_sel_hi:[1,0,0] neg_lo:[1,0,0] neg_hi:[1,0,0]
	v_pk_fma_f16 v7, v3, v130, v131 op_sel:[0,0,0] op_sel_hi:[1,0,0] neg_lo:[1,0,0] neg_hi:[1,0,0]
	v_pk_fma_f16 v8, v4, v130, v131 op_sel:[0,0,0] op_sel_hi:[1,0,0] neg_lo:[1,0,0] neg_hi:[1,0,0]
	v_pk_fma_f16 v9, v5, v130, v131 op_sel:[0,0,0] op_sel_hi:[1,0,0] neg_lo:[1,0,0] neg_hi:[1,0,0]
	v_mfma_f32_16x16x32_f16 v[22:25], v[14:17], v[2:5], 0
	ds_read2_b64 v[92:95], v32 offset0:27 offset1:229
	s_waitcnt lgkmcnt(6)
	v_pk_fma_f16 v2, v68, v6, v2
	v_pk_fma_f16 v3, v69, v7, v3
	v_pk_fma_f16 v4, v70, v8, v4
	v_pk_fma_f16 v5, v71, v9, v5
	v_cndmask_b32_e64 v26, v26, v18, s[62:63]
	v_pk_fma_f16 v6, v2, v132, v133 op_sel:[0,0,0] op_sel_hi:[1,0,0] neg_lo:[1,0,0] neg_hi:[1,0,0]
	v_pk_fma_f16 v7, v3, v132, v133 op_sel:[0,0,0] op_sel_hi:[1,0,0] neg_lo:[1,0,0] neg_hi:[1,0,0]
	v_pk_fma_f16 v8, v4, v132, v133 op_sel:[0,0,0] op_sel_hi:[1,0,0] neg_lo:[1,0,0] neg_hi:[1,0,0]
	v_pk_fma_f16 v9, v5, v132, v133 op_sel:[0,0,0] op_sel_hi:[1,0,0] neg_lo:[1,0,0] neg_hi:[1,0,0]
	v_mfma_f32_16x16x32_f16 v[18:21], v[14:17], v[2:5], 0
	ds_read2_b64 v[96:99], v32 offset0:28 offset1:230
	ds_read_b128 v[144:147], v33 offset:224
	v_pk_fma_f16 v2, v72, v6, v2
	v_pk_fma_f16 v3, v73, v7, v3
	v_pk_fma_f16 v4, v74, v8, v4
	v_pk_fma_f16 v5, v75, v9, v5
	v_cndmask_b32_e64 v27, v27, v23, s[62:63]
	v_pk_fma_f16 v6, v2, v134, v135 op_sel:[0,0,0] op_sel_hi:[1,0,0] neg_lo:[1,0,0] neg_hi:[1,0,0]
	v_pk_fma_f16 v7, v3, v134, v135 op_sel:[0,0,0] op_sel_hi:[1,0,0] neg_lo:[1,0,0] neg_hi:[1,0,0]
	v_pk_fma_f16 v8, v4, v134, v135 op_sel:[0,0,0] op_sel_hi:[1,0,0] neg_lo:[1,0,0] neg_hi:[1,0,0]
	v_pk_fma_f16 v9, v5, v134, v135 op_sel:[0,0,0] op_sel_hi:[1,0,0] neg_lo:[1,0,0] neg_hi:[1,0,0]
	v_mfma_f32_16x16x32_f16 v[22:25], v[14:17], v[2:5], 0
	ds_read2_b64 v[100:103], v32 offset0:29 offset1:231
	s_waitcnt lgkmcnt(6)
	v_pk_fma_f16 v2, v76, v6, v2
	v_pk_fma_f16 v3, v77, v7, v3
	v_pk_fma_f16 v4, v78, v8, v4
	v_pk_fma_f16 v5, v79, v9, v5
	v_cndmask_b32_e64 v28, v28, v20, s[62:63]
	v_pk_fma_f16 v6, v2, v136, v137 op_sel:[0,0,0] op_sel_hi:[1,0,0] neg_lo:[1,0,0] neg_hi:[1,0,0]
	v_pk_fma_f16 v7, v3, v136, v137 op_sel:[0,0,0] op_sel_hi:[1,0,0] neg_lo:[1,0,0] neg_hi:[1,0,0]
	v_pk_fma_f16 v8, v4, v136, v137 op_sel:[0,0,0] op_sel_hi:[1,0,0] neg_lo:[1,0,0] neg_hi:[1,0,0]
	v_pk_fma_f16 v9, v5, v136, v137 op_sel:[0,0,0] op_sel_hi:[1,0,0] neg_lo:[1,0,0] neg_hi:[1,0,0]
	v_mfma_f32_16x16x32_f16 v[18:21], v[14:17], v[2:5], 0
	ds_read2_b64 v[104:107], v32 offset0:30 offset1:232
	ds_read_b128 v[148:151], v33 offset:240
	v_pk_fma_f16 v2, v80, v6, v2
	v_pk_fma_f16 v3, v81, v7, v3
	v_pk_fma_f16 v4, v82, v8, v4
	v_pk_fma_f16 v5, v83, v9, v5
	v_cndmask_b32_e64 v29, v29, v25, s[62:63]
	v_readfirstlane_b32 s4, v37
	v_readfirstlane_b32 s5, v38
	s_and_b32 s4, s4, s5
	s_cbranch_scc0 .Lc0_slow1
.Lc0_back1:
	v_pk_fma_f16 v6, v2, v138, v139 op_sel:[0,0,0] op_sel_hi:[1,0,0] neg_lo:[1,0,0] neg_hi:[1,0,0]
	v_pk_fma_f16 v7, v3, v138, v139 op_sel:[0,0,0] op_sel_hi:[1,0,0] neg_lo:[1,0,0] neg_hi:[1,0,0]
	v_pk_fma_f16 v8, v4, v138, v139 op_sel:[0,0,0] op_sel_hi:[1,0,0] neg_lo:[1,0,0] neg_hi:[1,0,0]
	v_pk_fma_f16 v9, v5, v138, v139 op_sel:[0,0,0] op_sel_hi:[1,0,0] neg_lo:[1,0,0] neg_hi:[1,0,0]
	v_mfma_f32_16x16x32_f16 v[22:25], v[14:17], v[2:5], 0
	ds_read2_b64 v[108:111], v32 offset0:31 offset1:233
	s_waitcnt lgkmcnt(6)
	v_pk_fma_f16 v2, v84, v6, v2
	v_pk_fma_f16 v3, v85, v7, v3
	v_pk_fma_f16 v4, v86, v8, v4
	v_pk_fma_f16 v5, v87, v9, v5
	v_cndmask_b32_e64 v26, v26, v18, s[64:65]
	v_pk_fma_f16 v6, v2, v140, v141 op_sel:[0,0,0] op_sel_hi:[1,0,0] neg_lo:[1,0,0] neg_hi:[1,0,0]
	v_pk_fma_f16 v7, v3, v140, v141 op_sel:[0,0,0] op_sel_hi:[1,0,0] neg_lo:[1,0,0] neg_hi:[1,0,0]
	v_pk_fma_f16 v8, v4, v140, v141 op_sel:[0,0,0] op_sel_hi:[1,0,0] neg_lo:[1,0,0] neg_hi:[1,0,0]
	v_pk_fma_f16 v9, v5, v140, v141 op_sel:[0,0,0] op_sel_hi:[1,0,0] neg_lo:[1,0,0] neg_hi:[1,0,0]
	v_mfma_f32_16x16x32_f16 v[18:21], v[14:17], v[2:5], 0
	ds_read2_b64 v[48:51], v32 offset0:32 offset1:234
	ds_read_b128 v[120:123], v33 offset:256
	ds_read2_b64 v[10:13], v34 offset0:32 offset1:234
	v_pk_fma_f16 v2, v88, v6, v2
	v_pk_fma_f16 v3, v89, v7, v3
	v_pk_fma_f16 v4, v90, v8, v4
	v_pk_fma_f16 v5, v91, v9, v5
	v_cndmask_b32_e64 v27, v27, v23, s[64:65]
	v_pk_fma_f16 v6, v2, v142, v143 op_sel:[0,0,0] op_sel_hi:[1,0,0] neg_lo:[1,0,0] neg_hi:[1,0,0]
	v_pk_fma_f16 v7, v3, v142, v143 op_sel:[0,0,0] op_sel_hi:[1,0,0] neg_lo:[1,0,0] neg_hi:[1,0,0]
	v_pk_fma_f16 v8, v4, v142, v143 op_sel:[0,0,0] op_sel_hi:[1,0,0] neg_lo:[1,0,0] neg_hi:[1,0,0]
	v_pk_fma_f16 v9, v5, v142, v143 op_sel:[0,0,0] op_sel_hi:[1,0,0] neg_lo:[1,0,0] neg_hi:[1,0,0]
	v_mfma_f32_16x16x32_f16 v[22:25], v[14:17], v[2:5], 0
	ds_read2_b64 v[52:55], v32 offset0:33 offset1:235
	s_waitcnt lgkmcnt(7)
	v_pk_fma_f16 v2, v92, v6, v2
	v_pk_fma_f16 v3, v93, v7, v3
	v_pk_fma_f16 v4, v94, v8, v4
	v_pk_fma_f16 v5, v95, v9, v5
	v_cndmask_b32_e64 v28, v28, v20, s[64:65]
	v_pk_fma_f16 v6, v2, v144, v145 op_sel:[0,0,0] op_sel_hi:[1,0,0] neg_lo:[1,0,0] neg_hi:[1,0,0]
	v_pk_fma_f16 v7, v3, v144, v145 op_sel:[0,0,0] op_sel_hi:[1,0,0] neg_lo:[1,0,0] neg_hi:[1,0,0]
	v_pk_fma_f16 v8, v4, v144, v145 op_sel:[0,0,0] op_sel_hi:[1,0,0] neg_lo:[1,0,0] neg_hi:[1,0,0]
	v_pk_fma_f16 v9, v5, v144, v145 op_sel:[0,0,0] op_sel_hi:[1,0,0] neg_lo:[1,0,0] neg_hi:[1,0,0]
	v_mfma_f32_16x16x32_f16 v[18:21], v[14:17], v[2:5], 0
	ds_read2_b64 v[56:59], v32 offset0:34 offset1:236
	ds_read_b128 v[124:127], v33 offset:272
	v_pk_fma_f16 v2, v96, v6, v2
	v_pk_fma_f16 v3, v97, v7, v3
	v_pk_fma_f16 v4, v98, v8, v4
	v_pk_fma_f16 v5, v99, v9, v5
	v_cndmask_b32_e64 v29, v29, v25, s[64:65]
	v_pk_fma_f16 v6, v2, v146, v147 op_sel:[0,0,0] op_sel_hi:[1,0,0] neg_lo:[1,0,0] neg_hi:[1,0,0]
	v_pk_fma_f16 v7, v3, v146, v147 op_sel:[0,0,0] op_sel_hi:[1,0,0] neg_lo:[1,0,0] neg_hi:[1,0,0]
	v_pk_fma_f16 v8, v4, v146, v147 op_sel:[0,0,0] op_sel_hi:[1,0,0] neg_lo:[1,0,0] neg_hi:[1,0,0]
	v_pk_fma_f16 v9, v5, v146, v147 op_sel:[0,0,0] op_sel_hi:[1,0,0] neg_lo:[1,0,0] neg_hi:[1,0,0]
	v_mfma_f32_16x16x32_f16 v[22:25], v[14:17], v[2:5], 0
	ds_read2_b64 v[60:63], v32 offset0:35 offset1:237
	s_waitcnt lgkmcnt(7)
	v_pk_fma_f16 v2, v100, v6, v2
	v_pk_fma_f16 v3, v101, v7, v3
	v_pk_fma_f16 v4, v102, v8, v4
	v_pk_fma_f16 v5, v103, v9, v5
	v_cndmask_b32_e64 v26, v26, v18, s[66:67]
	v_pk_fma_f16 v6, v2, v148, v149 op_sel:[0,0,0] op_sel_hi:[1,0,0] neg_lo:[1,0,0] neg_hi:[1,0,0]
	v_pk_fma_f16 v7, v3, v148, v149 op_sel:[0,0,0] op_sel_hi:[1,0,0] neg_lo:[1,0,0] neg_hi:[1,0,0]
	v_pk_fma_f16 v8, v4, v148, v149 op_sel:[0,0,0] op_sel_hi:[1,0,0] neg_lo:[1,0,0] neg_hi:[1,0,0]
	v_pk_fma_f16 v9, v5, v148, v149 op_sel:[0,0,0] op_sel_hi:[1,0,0] neg_lo:[1,0,0] neg_hi:[1,0,0]
	v_mfma_f32_16x16x32_f16 v[18:21], v[14:17], v[2:5], 0
	ds_read2_b64 v[64:67], v32 offset0:36 offset1:238
	ds_read_b128 v[128:131], v33 offset:288
	v_pk_fma_f16 v2, v104, v6, v2
	v_pk_fma_f16 v3, v105, v7, v3
	v_pk_fma_f16 v4, v106, v8, v4
	v_pk_fma_f16 v5, v107, v9, v5
	v_cndmask_b32_e64 v27, v27, v23, s[66:67]
	v_pk_fma_f16 v6, v2, v150, v151 op_sel:[0,0,0] op_sel_hi:[1,0,0] neg_lo:[1,0,0] neg_hi:[1,0,0]
	v_pk_fma_f16 v7, v3, v150, v151 op_sel:[0,0,0] op_sel_hi:[1,0,0] neg_lo:[1,0,0] neg_hi:[1,0,0]
	v_pk_fma_f16 v8, v4, v150, v151 op_sel:[0,0,0] op_sel_hi:[1,0,0] neg_lo:[1,0,0] neg_hi:[1,0,0]
	v_pk_fma_f16 v9, v5, v150, v151 op_sel:[0,0,0] op_sel_hi:[1,0,0] neg_lo:[1,0,0] neg_hi:[1,0,0]
	v_mfma_f32_16x16x32_f16 v[22:25], v[14:17], v[2:5], 0
	ds_read2_b64 v[68:71], v32 offset0:37 offset1:239
	s_waitcnt lgkmcnt(6)
	v_pk_fma_f16 v2, v108, v6, v2
	v_pk_fma_f16 v3, v109, v7, v3
	v_pk_fma_f16 v4, v110, v8, v4
	v_pk_fma_f16 v5, v111, v9, v5
	v_cndmask_b32_e64 v28, v28, v20, s[66:67]
.Lc0_next1:
	v_add_u32_e32 v32, 0x100, v32
	v_add_u32_e32 v33, 0x100, v33
	v_add_u32_e32 v34, 0x100, v34
	v_add_u32_e32 v36, 8, v36
	v_add_u32_e32 v39, 0x1000, v39
	v_add_u32_e32 v43, 0x1000, v43
	v_add_u32_e32 v35, 0x800, v35
	s_xor_b32 s71, s71, 2
	s_add_i32 s70, s70, 1
	s_cmp_lt_u32 s70, 6
	s_cbranch_scc1 .Lc0_loop
	v_pk_fma_f16 v6, v2, v120, v121 op_sel:[0,0,0] op_sel_hi:[1,0,0] neg_lo:[1,0,0] neg_hi:[1,0,0]
	v_pk_fma_f16 v7, v3, v120, v121 op_sel:[0,0,0] op_sel_hi:[1,0,0] neg_lo:[1,0,0] neg_hi:[1,0,0]
	v_pk_fma_f16 v8, v4, v120, v121 op_sel:[0,0,0] op_sel_hi:[1,0,0] neg_lo:[1,0,0] neg_hi:[1,0,0]
	v_pk_fma_f16 v9, v5, v120, v121 op_sel:[0,0,0] op_sel_hi:[1,0,0] neg_lo:[1,0,0] neg_hi:[1,0,0]
	v_mfma_f32_16x16x32_f16 v[18:21], v[10:13], v[2:5], 0
	ds_read2_b64 v[72:75], v32 offset0:6 offset1:208
	ds_read_b128 v[132:135], v33 offset:48
	v_pk_fma_f16 v2, v48, v6, v2
	v_pk_fma_f16 v3, v49, v7, v3
	v_pk_fma_f16 v4, v50, v8, v4
	v_pk_fma_f16 v5, v51, v9, v5
	v_cndmask_b32_e64 v29, v29, v25, s[66:67]
	v_cvt_pk_f16_f32 v30, v26, v27
	v_cvt_pk_f16_f32 v31, v28, v29
	ds_write_b16 v39, v30 offset:0
	ds_write_b16_d16_hi v39, v30 offset:64
	ds_write_b16 v39, v31 offset:128
	ds_write_b16_d16_hi v39, v31 offset:192
	s_mov_b64 exec, 1
	ds_add_u32 v36, v44 offset:124
	s_mov_b64 exec, -1
	v_pk_fma_f16 v6, v2, v122, v123 op_sel:[0,0,0] op_sel_hi:[1,0,0] neg_lo:[1,0,0] neg_hi:[1,0,0]
	v_pk_fma_f16 v7, v3, v122, v123 op_sel:[0,0,0] op_sel_hi:[1,0,0] neg_lo:[1,0,0] neg_hi:[1,0,0]
	v_pk_fma_f16 v8, v4, v122, v123 op_sel:[0,0,0] op_sel_hi:[1,0,0] neg_lo:[1,0,0] neg_hi:[1,0,0]
	v_pk_fma_f16 v9, v5, v122, v123 op_sel:[0,0,0] op_sel_hi:[1,0,0] neg_lo:[1,0,0] neg_hi:[1,0,0]
	v_mfma_f32_16x16x32_f16 v[22:25], v[10:13], v[2:5], 0
	ds_read2_b64 v[76:79], v32 offset0:7 offset1:209
	s_waitcnt lgkmcnt(11)
	v_pk_fma_f16 v2, v52, v6, v2
	v_pk_fma_f16 v3, v53, v7, v3
	v_pk_fma_f16 v4, v54, v8, v4
	v_pk_fma_f16 v5, v55, v9, v5
	v_cndmask_b32_e64 v26, v26, v18, s[60:61]
	v_pk_fma_f16 v6, v2, v124, v125 op_sel:[0,0,0] op_sel_hi:[1,0,0] neg_lo:[1,0,0] neg_hi:[1,0,0]
	v_pk_fma_f16 v7, v3, v124, v125 op_sel:[0,0,0] op_sel_hi:[1,0,0] neg_lo:[1,0,0] neg_hi:[1,0,0]
	v_pk_fma_f16 v8, v4, v124, v125 op_sel:[0,0,0] op_sel_hi:[1,0,0] neg_lo:[1,0,0] neg_hi:[1,0,0]
	v_pk_fma_f16 v9, v5, v124, v125 op_sel:[0,0,0] op_sel_hi:[1,0,0] neg_lo:[1,0,0] neg_hi:[1,0,0]
	v_mfma_f32_16x16x32_f16 v[18:21], v[10:13], v[2:5], 0
	v_pk_fma_f16 v2, v56, v6, v2
	v_pk_fma_f16 v3, v57, v7, v3
	v_pk_fma_f16 v4, v58, v8, v4
	v_pk_fma_f16 v5, v59, v9, v5
	v_cndmask_b32_e64 v27, v27, v23, s[60:61]
	v_pk_fma_f16 v6, v2, v126, v127 op_sel:[0,0,0] op_sel_hi:[1,0,0] neg_lo:[1,0,0] neg_hi:[1,0,0]
	v_pk_fma_f16 v7, v3, v126, v127 op_sel:[0,0,0] op_sel_hi:[1,0,0] neg_lo:[1,0,0] neg_hi:[1,0,0]
	v_pk_fma_f16 v8, v4, v126, v127 op_sel:[0,0,0] op_sel_hi:[1,0,0] neg_lo:[1,0,0] neg_hi:[1,0,0]
	v_pk_fma_f16 v9, v5, v126, v127 op_sel:[0,0,0] op_sel_hi:[1,0,0] neg_lo:[1,0,0] neg_hi:[1,0,0]
	v_mfma_f32_16x16x32_f16 v[22:25], v[10:13], v[2:5], 0
	s_waitcnt lgkmcnt(8)
	v_pk_fma_f16 v2, v60, v6, v2
	v_pk_fma_f16 v3, v61, v7, v3
	v_pk_fma_f16 v4, v62, v8, v4
	v_pk_fma_f16 v5, v63, v9, v5
	v_cndmask_b32_e64 v28, v28, v20, s[60:61]
	v_pk_fma_f16 v6, v2, v128, v129 op_sel:[0,0,0] op_sel_hi:[1,0,0] neg_lo:[1,0,0] neg_hi:[1,0,0]
	v_pk_fma_f16 v7, v3, v128, v129 op_sel:[0,0,0] op_sel_hi:[1,0,0] neg_lo:[1,0,0] neg_hi:[1,0,0]
	v_pk_fma_f16 v8, v4, v128, v129 op_sel:[0,0,0] op_sel_hi:[1,0,0] neg_lo:[1,0,0] neg_hi:[1,0,0]
	v_pk_fma_f16 v9, v5, v128, v129 op_sel:[0,0,0] op_sel_hi:[1,0,0] neg_lo:[1,0,0] neg_hi:[1,0,0]
	v_mfma_f32_16x16x32_f16 v[18:21], v[10:13], v[2:5], 0
	v_pk_fma_f16 v2, v64, v6, v2
	v_pk_fma_f16 v3, v65, v7, v3
	v_pk_fma_f16 v4, v66, v8, v4
	v_pk_fma_f16 v5, v67, v9, v5
	v_cndmask_b32_e64 v29, v29, v25, s[60:61]
	v_pk_fma_f16 v6, v2, v130, v131 op_sel:[0,0,0] op_sel_hi:[1,0,0] neg_lo:[1,0,0] neg_hi:[1,0,0]
	v_pk_fma_f16 v7, v3, v130, v131 op_sel:[0,0,0] op_sel_hi:[1,0,0] neg_lo:[1,0,0] neg_hi:[1,0,0]
	v_pk_fma_f16 v8, v4, v130, v131 op_sel:[0,0,0] op_sel_hi:[1,0,0] neg_lo:[1,0,0] neg_hi:[1,0,0]
	v_pk_fma_f16 v9, v5, v130, v131 op_sel:[0,0,0] op_sel_hi:[1,0,0] neg_lo:[1,0,0] neg_hi:[1,0,0]
	v_mfma_f32_16x16x32_f16 v[22:25], v[10:13], v[2:5], 0
	s_waitcnt lgkmcnt(0)
	v_pk_fma_f16 v2, v68, v6, v2
	v_pk_fma_f16 v3, v69, v7, v3
	v_pk_fma_f16 v4, v70, v8, v4
	v_pk_fma_f16 v5, v71, v9, v5
	v_cndmask_b32_e64 v26, v26, v18, s[62:63]
	v_pk_fma_f16 v6, v2, v132, v133 op_sel:[0,0,0] op_sel_hi:[1,0,0] neg_lo:[1,0,0] neg_hi:[1,0,0]
	v_pk_fma_f16 v7, v3, v132, v133 op_sel:[0,0,0] op_sel_hi:[1,0,0] neg_lo:[1,0,0] neg_hi:[1,0,0]
	v_pk_fma_f16 v8, v4, v132, v133 op_sel:[0,0,0] op_sel_hi:[1,0,0] neg_lo:[1,0,0] neg_hi:[1,0,0]
	v_pk_fma_f16 v9, v5, v132, v133 op_sel:[0,0,0] op_sel_hi:[1,0,0] neg_lo:[1,0,0] neg_hi:[1,0,0]
	v_mfma_f32_16x16x32_f16 v[18:21], v[10:13], v[2:5], 0
	v_pk_fma_f16 v2, v72, v6, v2
	v_pk_fma_f16 v3, v73, v7, v3
	v_pk_fma_f16 v4, v74, v8, v4
	v_pk_fma_f16 v5, v75, v9, v5
	v_cndmask_b32_e64 v27, v27, v23, s[62:63]
	v_pk_fma_f16 v6, v2, v134, v135 op_sel:[0,0,0] op_sel_hi:[1,0,0] neg_lo:[1,0,0] neg_hi:[1,0,0]
	v_pk_fma_f16 v7, v3, v134, v135 op_sel:[0,0,0] op_sel_hi:[1,0,0] neg_lo:[1,0,0] neg_hi:[1,0,0]
	v_pk_fma_f16 v8, v4, v134, v135 op_sel:[0,0,0] op_sel_hi:[1,0,0] neg_lo:[1,0,0] neg_hi:[1,0,0]
	v_pk_fma_f16 v9, v5, v134, v135 op_sel:[0,0,0] op_sel_hi:[1,0,0] neg_lo:[1,0,0] neg_hi:[1,0,0]
	v_mfma_f32_16x16x32_f16 v[22:25], v[10:13], v[2:5], 0
	v_pk_fma_f16 v2, v76, v6, v2
	v_pk_fma_f16 v3, v77, v7, v3
	v_pk_fma_f16 v4, v78, v8, v4
	v_pk_fma_f16 v5, v79, v9, v5
	v_cndmask_b32_e64 v28, v28, v20, s[62:63]
	s_nop 7
	v_cndmask_b32_e64 v29, v29, v25, s[62:63]
	v_cvt_pk_f16_f32 v30, v26, v27
	v_cvt_pk_f16_f32 v31, v28, v29
	ds_write_b16 v39, v30 offset:2048
	ds_write_b16_d16_hi v39, v30 offset:2112
	ds_write_b16 v39, v31 offset:2176
	ds_write_b16_d16_hi v39, v31 offset:2240
	s_mov_b64 exec, 1
	ds_add_u32 v36, v44 offset:128
	s_mov_b64 exec, -1
	s_branch .Lc0_end

.Lc_par1:
	ds_read2_b64 v[48:51], v32 offset0:0 offset1:202
	ds_read_b128 v[120:123], v33 offset:0
	ds_read2_b64 v[10:13], v34 offset0:0 offset1:202
	ds_read2_b64 v[52:55], v32 offset0:1 offset1:203
	ds_read2_b64 v[56:59], v32 offset0:2 offset1:204
	ds_read_b128 v[124:127], v33 offset:16
	ds_read2_b64 v[60:63], v32 offset0:3 offset1:205
	ds_read2_b64 v[64:67], v32 offset0:4 offset1:206
	ds_read_b128 v[128:131], v33 offset:32
	ds_read2_b64 v[68:71], v32 offset0:5 offset1:207
	s_mov_b32 s70, 0
	s_mov_b32 s71, 0
	s_waitcnt lgkmcnt(6)
.Lc1_loop:
	v_pk_fma_f16 v6, v2, v120, v121 op_sel:[0,1,1] op_sel_hi:[1,1,1] neg_lo:[1,0,0] neg_hi:[1,0,0]
	v_pk_fma_f16 v7, v3, v120, v121 op_sel:[0,1,1] op_sel_hi:[1,1,1] neg_lo:[1,0,0] neg_hi:[1,0,0]
	v_pk_fma_f16 v8, v4, v120, v121 op_sel:[0,1,1] op_sel_hi:[1,1,1] neg_lo:[1,0,0] neg_hi:[1,0,0]
	v_pk_fma_f16 v9, v5, v120, v121 op_sel:[0,1,1] op_sel_hi:[1,1,1] neg_lo:[1,0,0] neg_hi:[1,0,0]
	v_mfma_f32_16x16x32_f16 v[18:21], v[10:13], v[2:5], 0
	ds_read2_b64 v[72:75], v32 offset0:6 offset1:208
	ds_read_b128 v[132:135], v33 offset:48
	ds_read_b32 v37, v36 offset:4
	ds_read_b32 v38, v36 offset:68
	v_pk_fma_f16 v2, v48, v6, v2
	v_pk_fma_f16 v3, v49, v7, v3
	v_pk_fma_f16 v4, v50, v8, v4
	v_pk_fma_f16 v5, v51, v9, v5
	v_cndmask_b32_e64 v29, v29, v25, s[66:67]
	v_cvt_pk_f16_f32 v30, v26, v27
	v_cvt_pk_f16_f32 v31, v28, v29
	ds_write_b16 v39, v30 offset:0
	ds_write_b16_d16_hi v39, v30 offset:64
	ds_write_b16 v39, v31 offset:128
	ds_write_b16_d16_hi v39, v31 offset:192
	s_mov_b64 exec, 1
	ds_add_u32 v36, v44 offset:124
	s_mov_b64 exec, -1
	v_pk_fma_f16 v6, v2, v122, v123 op_sel:[0,1,1] op_sel_hi:[1,1,1] neg_lo:[1,0,0] neg_hi:[1,0,0]
	v_pk_fma_f16 v7, v3, v122, v123 op_sel:[0,1,1] op_sel_hi:[1,1,1] neg_lo:[1,0,0] neg_hi:[1,0,0]
	v_pk_fma_f16 v8, v4, v122, v123 op_sel:[0,1,1] op_sel_hi:[1,1,1] neg_lo:[1,0,0] neg_hi:[1,0,0]
	v_pk_fma_f16 v9, v5, v122, v123 op_sel:[0,1,1] op_sel_hi:[1,1,1] neg_lo:[1,0,0] neg_hi:[1,0,0]
	v_mfma_f32_16x16x32_f16 v[22:25], v[10:13], v[2:5], 0
	ds_read2_b64 v[76:79], v32 offset0:7 offset1:209
	s_waitcnt lgkmcnt(13)
	v_pk_fma_f16 v2, v52, v6, v2
	v_pk_fma_f16 v3, v53, v7, v3
	v_pk_fma_f16 v4, v54, v8, v4
	v_pk_fma_f16 v5, v55, v9, v5
	v_cndmask_b32_e64 v26, v26, v18, s[60:61]
	v_pk_fma_f16 v6, v2, v124, v125 op_sel:[0,1,1] op_sel_hi:[1,1,1] neg_lo:[1,0,0] neg_hi:[1,0,0]
	v_pk_fma_f16 v7, v3, v124, v125 op_sel:[0,1,1] op_sel_hi:[1,1,1] neg_lo:[1,0,0] neg_hi:[1,0,0]
	v_pk_fma_f16 v8, v4, v124, v125 op_sel:[0,1,1] op_sel_hi:[1,1,1] neg_lo:[1,0,0] neg_hi:[1,0,0]
	v_pk_fma_f16 v9, v5, v124, v125 op_sel:[0,1,1] op_sel_hi:[1,1,1] neg_lo:[1,0,0] neg_hi:[1,0,0]
	v_mfma_f32_16x16x32_f16 v[18:21], v[10:13], v[2:5], 0
	ds_read2_b64 v[80:83], v32 offset0:8 offset1:210
	ds_read_b128 v[136:139], v33 offset:64
	v_pk_fma_f16 v2, v56, v6, v2
	v_pk_fma_f16 v3, v57, v7, v3
	v_pk_fma_f16 v4, v58, v8, v4
	v_pk_fma_f16 v5, v59, v9, v5
	v_cndmask_b32_e64 v27, v27, v23, s[60:61]
	v_pk_fma_f16 v6, v2, v126, v127 op_sel:[0,1,1] op_sel_hi:[1,1,1] neg_lo:[1,0,0] neg_hi:[1,0,0]
	v_pk_fma_f16 v7, v3, v126, v127 op_sel:[0,1,1] op_sel_hi:[1,1,1] neg_lo:[1,0,0] neg_hi:[1,0,0]
	v_pk_fma_f16 v8, v4, v126, v127 op_sel:[0,1,1] op_sel_hi:[1,1,1] neg_lo:[1,0,0] neg_hi:[1,0,0]
	v_pk_fma_f16 v9, v5, v126, v127 op_sel:[0,1,1] op_sel_hi:[1,1,1] neg_lo:[1,0,0] neg_hi:[1,0,0]
	v_mfma_f32_16x16x32_f16 v[22:25], v[10:13], v[2:5], 0
	ds_read2_b64 v[84:87], v32 offset0:9 offset1:211
	s_waitcnt lgkmcnt(13)
	v_pk_fma_f16 v2, v60, v6, v2
	v_pk_fma_f16 v3, v61, v7, v3
	v_pk_fma_f16 v4, v62, v8, v4
	v_pk_fma_f16 v5, v63, v9, v5
	v_cndmask_b32_e64 v28, v28, v20, s[60:61]
	v_pk_fma_f16 v6, v2, v128, v129 op_sel:[0,1,1] op_sel_hi:[1,1,1] neg_lo:[1,0,0] neg_hi:[1,0,0]
	v_pk_fma_f16 v7, v3, v128, v129 op_sel:[0,1,1] op_sel_hi:[1,1,1] neg_lo:[1,0,0] neg_hi:[1,0,0]
	v_pk_fma_f16 v8, v4, v128, v129 op_sel:[0,1,1] op_sel_hi:[1,1,1] neg_lo:[1,0,0] neg_hi:[1,0,0]
	v_pk_fma_f16 v9, v5, v128, v129 op_sel:[0,1,1] op_sel_hi:[1,1,1] neg_lo:[1,0,0] neg_hi:[1,0,0]
	v_mfma_f32_16x16x32_f16 v[18:21], v[10:13], v[2:5], 0
	ds_read2_b64 v[88:91], v32 offset0:10 offset1:212
	ds_read_b128 v[140:143], v33 offset:80
	v_pk_fma_f16 v2, v64, v6, v2
	v_pk_fma_f16 v3, v65, v7, v3
	v_pk_fma_f16 v4, v66, v8, v4
	v_pk_fma_f16 v5, v67, v9, v5
	v_cndmask_b32_e64 v29, v29, v25, s[60:61]
	v_pk_fma_f16 v6, v2, v130, v131 op_sel:[0,1,1] op_sel_hi:[1,1,1] neg_lo:[1,0,0] neg_hi:[1,0,0]
	v_pk_fma_f16 v7, v3, v130, v131 op_sel:[0,1,1] op_sel_hi:[1,1,1] neg_lo:[1,0,0] neg_hi:[1,0,0]
	v_pk_fma_f16 v8, v4, v130, v131 op_sel:[0,1,1] op_sel_hi:[1,1,1] neg_lo:[1,0,0] neg_hi:[1,0,0]
	v_pk_fma_f16 v9, v5, v130, v131 op_sel:[0,1,1] op_sel_hi:[1,1,1] neg_lo:[1,0,0] neg_hi:[1,0,0]
	v_mfma_f32_16x16x32_f16 v[22:25], v[10:13], v[2:5], 0
	ds_read2_b64 v[92:95], v32 offset0:11 offset1:213
	s_waitcnt lgkmcnt(6)
	v_pk_fma_f16 v2, v68, v6, v2
	v_pk_fma_f16 v3, v69, v7, v3
	v_pk_fma_f16 v4, v70, v8, v4
	v_pk_fma_f16 v5, v71, v9, v5
	v_cndmask_b32_e64 v26, v26, v18, s[62:63]
	v_pk_fma_f16 v6, v2, v132, v133 op_sel:[0,1,1] op_sel_hi:[1,1,1] neg_lo:[1,0,0] neg_hi:[1,0,0]
	v_pk_fma_f16 v7, v3, v132, v133 op_sel:[0,1,1] op_sel_hi:[1,1,1] neg_lo:[1,0,0] neg_hi:[1,0,0]
	v_pk_fma_f16 v8, v4, v132, v133 op_sel:[0,1,1] op_sel_hi:[1,1,1] neg_lo:[1,0,0] neg_hi:[1,0,0]
	v_pk_fma_f16 v9, v5, v132, v133 op_sel:[0,1,1] op_sel_hi:[1,1,1] neg_lo:[1,0,0] neg_hi:[1,0,0]
	v_mfma_f32_16x16x32_f16 v[18:21], v[10:13], v[2:5], 0
	ds_read2_b64 v[96:99], v32 offset0:12 offset1:214
	ds_read_b128 v[144:147], v33 offset:96
	v_pk_fma_f16 v2, v72, v6, v2
	v_pk_fma_f16 v3, v73, v7, v3
	v_pk_fma_f16 v4, v74, v8, v4
	v_pk_fma_f16 v5, v75, v9, v5
	v_cndmask_b32_e64 v27, v27, v23, s[62:63]
	v_pk_fma_f16 v6, v2, v134, v135 op_sel:[0,1,1] op_sel_hi:[1,1,1] neg_lo:[1,0,0] neg_hi:[1,0,0]
	v_pk_fma_f16 v7, v3, v134, v135 op_sel:[0,1,1] op_sel_hi:[1,1,1] neg_lo:[1,0,0] neg_hi:[1,0,0]
	v_pk_fma_f16 v8, v4, v134, v135 op_sel:[0,1,1] op_sel_hi:[1,1,1] neg_lo:[1,0,0] neg_hi:[1,0,0]
	v_pk_fma_f16 v9, v5, v134, v135 op_sel:[0,1,1] op_sel_hi:[1,1,1] neg_lo:[1,0,0] neg_hi:[1,0,0]
	v_mfma_f32_16x16x32_f16 v[22:25], v[10:13], v[2:5], 0
	ds_read2_b64 v[100:103], v32 offset0:13 offset1:215
	s_waitcnt lgkmcnt(6)
	v_pk_fma_f16 v2, v76, v6, v2
	v_pk_fma_f16 v3, v77, v7, v3
	v_pk_fma_f16 v4, v78, v8, v4
	v_pk_fma_f16 v5, v79, v9, v5
	v_cndmask_b32_e64 v28, v28, v20, s[62:63]
	v_pk_fma_f16 v6, v2, v136, v137 op_sel:[0,1,1] op_sel_hi:[1,1,1] neg_lo:[1,0,0] neg_hi:[1,0,0]
	v_pk_fma_f16 v7, v3, v136, v137 op_sel:[0,1,1] op_sel_hi:[1,1,1] neg_lo:[1,0,0] neg_hi:[1,0,0]
	v_pk_fma_f16 v8, v4, v136, v137 op_sel:[0,1,1] op_sel_hi:[1,1,1] neg_lo:[1,0,0] neg_hi:[1,0,0]
	v_pk_fma_f16 v9, v5, v136, v137 op_sel:[0,1,1] op_sel_hi:[1,1,1] neg_lo:[1,0,0] neg_hi:[1,0,0]
	v_mfma_f32_16x16x32_f16 v[18:21], v[10:13], v[2:5], 0
	ds_read2_b64 v[104:107], v32 offset0:14 offset1:216
	ds_read_b128 v[148:151], v33 offset:112
	v_pk_fma_f16 v2, v80, v6, v2
	v_pk_fma_f16 v3, v81, v7, v3
	v_pk_fma_f16 v4, v82, v8, v4
	v_pk_fma_f16 v5, v83, v9, v5
	v_cndmask_b32_e64 v29, v29, v25, s[62:63]
	v_readfirstlane_b32 s4, v37
	v_readfirstlane_b32 s5, v38
	s_and_b32 s4, s4, s5
	s_cbranch_scc0 .Lc1_slow0

.Lc1_nd0:
	v_pk_fma_f16 v6, v2, v138, v139 op_sel:[0,1,1] op_sel_hi:[1,1,1] neg_lo:[1,0,0] neg_hi:[1,0,0]
	v_pk_fma_f16 v7, v3, v138, v139 op_sel:[0,1,1] op_sel_hi:[1,1,1] neg_lo:[1,0,0] neg_hi:[1,0,0]
	v_pk_fma_f16 v8, v4, v138, v139 op_sel:[0,1,1] op_sel_hi:[1,1,1] neg_lo:[1,0,0] neg_hi:[1,0,0]
	v_pk_fma_f16 v9, v5, v138, v139 op_sel:[0,1,1] op_sel_hi:[1,1,1] neg_lo:[1,0,0] neg_hi:[1,0,0]
	v_mfma_f32_16x16x32_f16 v[22:25], v[10:13], v[2:5], 0
	ds_read2_b64 v[108:111], v32 offset0:15 offset1:217
	s_waitcnt lgkmcnt(6)
	v_pk_fma_f16 v2, v84, v6, v2
	v_pk_fma_f16 v3, v85, v7, v3
	v_pk_fma_f16 v4, v86, v8, v4
	v_pk_fma_f16 v5, v87, v9, v5
	v_cndmask_b32_e64 v26, v26, v18, s[64:65]
	v_pk_fma_f16 v6, v2, v140, v141 op_sel:[0,1,1] op_sel_hi:[1,1,1] neg_lo:[1,0,0] neg_hi:[1,0,0]
	v_pk_fma_f16 v7, v3, v140, v141 op_sel:[0,1,1] op_sel_hi:[1,1,1] neg_lo:[1,0,0] neg_hi:[1,0,0]
	v_pk_fma_f16 v8, v4, v140, v141 op_sel:[0,1,1] op_sel_hi:[1,1,1] neg_lo:[1,0,0] neg_hi:[1,0,0]
	v_pk_fma_f16 v9, v5, v140, v141 op_sel:[0,1,1] op_sel_hi:[1,1,1] neg_lo:[1,0,0] neg_hi:[1,0,0]
	v_mfma_f32_16x16x32_f16 v[18:21], v[10:13], v[2:5], 0
	ds_read2_b64 v[48:51], v32 offset0:16 offset1:218
	ds_read_b128 v[120:123], v33 offset:128
	ds_read2_b64 v[14:17], v34 offset0:16 offset1:218
	v_pk_fma_f16 v2, v88, v6, v2
	v_pk_fma_f16 v3, v89, v7, v3
	v_pk_fma_f16 v4, v90, v8, v4
	v_pk_fma_f16 v5, v91, v9, v5
	v_cndmask_b32_e64 v27, v27, v23, s[64:65]
	v_pk_fma_f16 v6, v2, v142, v143 op_sel:[0,1,1] op_sel_hi:[1,1,1] neg_lo:[1,0,0] neg_hi:[1,0,0]
	v_pk_fma_f16 v7, v3, v142, v143 op_sel:[0,1,1] op_sel_hi:[1,1,1] neg_lo:[1,0,0] neg_hi:[1,0,0]
	v_pk_fma_f16 v8, v4, v142, v143 op_sel:[0,1,1] op_sel_hi:[1,1,1] neg_lo:[1,0,0] neg_hi:[1,0,0]
	v_pk_fma_f16 v9, v5, v142, v143 op_sel:[0,1,1] op_sel_hi:[1,1,1] neg_lo:[1,0,0] neg_hi:[1,0,0]
	v_mfma_f32_16x16x32_f16 v[22:25], v[10:13], v[2:5], 0
	ds_read2_b64 v[52:55], v32 offset0:17 offset1:219
	s_waitcnt lgkmcnt(7)
	v_pk_fma_f16 v2, v92, v6, v2
	v_pk_fma_f16 v3, v93, v7, v3
	v_pk_fma_f16 v4, v94, v8, v4
	v_pk_fma_f16 v5, v95, v9, v5
	v_cndmask_b32_e64 v28, v28, v20, s[64:65]
	v_pk_fma_f16 v6, v2, v144, v145 op_sel:[0,1,1] op_sel_hi:[1,1,1] neg_lo:[1,0,0] neg_hi:[1,0,0]
	v_pk_fma_f16 v7, v3, v144, v145 op_sel:[0,1,1] op_sel_hi:[1,1,1] neg_lo:[1,0,0] neg_hi:[1,0,0]
	v_pk_fma_f16 v8, v4, v144, v145 op_sel:[0,1,1] op_sel_hi:[1,1,1] neg_lo:[1,0,0] neg_hi:[1,0,0]
	v_pk_fma_f16 v9, v5, v144, v145 op_sel:[0,1,1] op_sel_hi:[1,1,1] neg_lo:[1,0,0] neg_hi:[1,0,0]
	v_mfma_f32_16x16x32_f16 v[18:21], v[10:13], v[2:5], 0
	ds_read2_b64 v[56:59], v32 offset0:18 offset1:220
	ds_read_b128 v[124:127], v33 offset:144
	v_pk_fma_f16 v2, v96, v6, v2
	v_pk_fma_f16 v3, v97, v7, v3
	v_pk_fma_f16 v4, v98, v8, v4
	v_pk_fma_f16 v5, v99, v9, v5
	v_cndmask_b32_e64 v29, v29, v25, s[64:65]
	s_cmp_eq_u32 s72, 1
	s_cbranch_scc0 .Lc1_ns0
	s_waitcnt lgkmcnt(7)
	v_readfirstlane_b32 s4, v45
	s_cmp_eq_u32 s4, 4
	s_cbranch_scc0 .Lc1_dslow0

.Lc1_ns0:
	v_pk_fma_f16 v6, v2, v146, v147 op_sel:[0,1,1] op_sel_hi:[1,1,1] neg_lo:[1,0,0] neg_hi:[1,0,0]
	v_pk_fma_f16 v7, v3, v146, v147 op_sel:[0,1,1] op_sel_hi:[1,1,1] neg_lo:[1,0,0] neg_hi:[1,0,0]
	v_pk_fma_f16 v8, v4, v146, v147 op_sel:[0,1,1] op_sel_hi:[1,1,1] neg_lo:[1,0,0] neg_hi:[1,0,0]
	v_pk_fma_f16 v9, v5, v146, v147 op_sel:[0,1,1] op_sel_hi:[1,1,1] neg_lo:[1,0,0] neg_hi:[1,0,0]
	v_mfma_f32_16x16x32_f16 v[22:25], v[10:13], v[2:5], 0
	ds_read2_b64 v[60:63], v32 offset0:19 offset1:221
	s_waitcnt lgkmcnt(7)
	v_pk_fma_f16 v2, v100, v6, v2
	v_pk_fma_f16 v3, v101, v7, v3
	v_pk_fma_f16 v4, v102, v8, v4
	v_pk_fma_f16 v5, v103, v9, v5
	v_cndmask_b32_e64 v26, v26, v18, s[66:67]
	v_pk_fma_f16 v6, v2, v148, v149 op_sel:[0,1,1] op_sel_hi:[1,1,1] neg_lo:[1,0,0] neg_hi:[1,0,0]
	v_pk_fma_f16 v7, v3, v148, v149 op_sel:[0,1,1] op_sel_hi:[1,1,1] neg_lo:[1,0,0] neg_hi:[1,0,0]
	v_pk_fma_f16 v8, v4, v148, v149 op_sel:[0,1,1] op_sel_hi:[1,1,1] neg_lo:[1,0,0] neg_hi:[1,0,0]
	v_pk_fma_f16 v9, v5, v148, v149 op_sel:[0,1,1] op_sel_hi:[1,1,1] neg_lo:[1,0,0] neg_hi:[1,0,0]
	v_mfma_f32_16x16x32_f16 v[18:21], v[10:13], v[2:5], 0
	ds_read2_b64 v[64:67], v32 offset0:20 offset1:222
	ds_read_b128 v[128:131], v33 offset:160
	v_pk_fma_f16 v2, v104, v6, v2
	v_pk_fma_f16 v3, v105, v7, v3
	v_pk_fma_f16 v4, v106, v8, v4
	v_pk_fma_f16 v5, v107, v9, v5
	v_cndmask_b32_e64 v27, v27, v23, s[66:67]
	v_pk_fma_f16 v6, v2, v150, v151 op_sel:[0,1,1] op_sel_hi:[1,1,1] neg_lo:[1,0,0] neg_hi:[1,0,0]
	v_pk_fma_f16 v7, v3, v150, v151 op_sel:[0,1,1] op_sel_hi:[1,1,1] neg_lo:[1,0,0] neg_hi:[1,0,0]
	v_pk_fma_f16 v8, v4, v150, v151 op_sel:[0,1,1] op_sel_hi:[1,1,1] neg_lo:[1,0,0] neg_hi:[1,0,0]
	v_pk_fma_f16 v9, v5, v150, v151 op_sel:[0,1,1] op_sel_hi:[1,1,1] neg_lo:[1,0,0] neg_hi:[1,0,0]
	v_mfma_f32_16x16x32_f16 v[22:25], v[10:13], v[2:5], 0
	ds_read2_b64 v[68:71], v32 offset0:21 offset1:223
	s_waitcnt lgkmcnt(6)
	v_pk_fma_f16 v2, v108, v6, v2
	v_pk_fma_f16 v3, v109, v7, v3
	v_pk_fma_f16 v4, v110, v8, v4
	v_pk_fma_f16 v5, v111, v9, v5
	v_cndmask_b32_e64 v28, v28, v20, s[66:67]
.Lc1_next0:
	v_pk_fma_f16 v6, v2, v120, v121 op_sel:[0,1,1] op_sel_hi:[1,1,1] neg_lo:[1,0,0] neg_hi:[1,0,0]
	v_pk_fma_f16 v7, v3, v120, v121 op_sel:[0,1,1] op_sel_hi:[1,1,1] neg_lo:[1,0,0] neg_hi:[1,0,0]
	v_pk_fma_f16 v8, v4, v120, v121 op_sel:[0,1,1] op_sel_hi:[1,1,1] neg_lo:[1,0,0] neg_hi:[1,0,0]
	v_pk_fma_f16 v9, v5, v120, v121 op_sel:[0,1,1] op_sel_hi:[1,1,1] neg_lo:[1,0,0] neg_hi:[1,0,0]
	v_mfma_f32_16x16x32_f16 v[18:21], v[14:17], v[2:5], 0
	ds_read2_b64 v[72:75], v32 offset0:22 offset1:224
	ds_read_b128 v[132:135], v33 offset:176
	ds_read_b32 v37, v36 offset:8
	ds_read_b32 v38, v36 offset:72
	v_pk_fma_f16 v2, v48, v6, v2
	v_pk_fma_f16 v3, v49, v7, v3
	v_pk_fma_f16 v4, v50, v8, v4
	v_pk_fma_f16 v5, v51, v9, v5
	v_cndmask_b32_e64 v29, v29, v25, s[66:67]
	v_cvt_pk_f16_f32 v30, v26, v27
	v_cvt_pk_f16_f32 v31, v28, v29
	ds_write_b16 v39, v30 offset:2048
	ds_write_b16_d16_hi v39, v30 offset:2112
	ds_write_b16 v39, v31 offset:2176
	ds_write_b16_d16_hi v39, v31 offset:2240
	s_mov_b64 exec, 1
	ds_add_u32 v36, v44 offset:128
	s_mov_b64 exec, -1
	v_pk_fma_f16 v6, v2, v122, v123 op_sel:[0,1,1] op_sel_hi:[1,1,1] neg_lo:[1,0,0] neg_hi:[1,0,0]
	v_pk_fma_f16 v7, v3, v122, v123 op_sel:[0,1,1] op_sel_hi:[1,1,1] neg_lo:[1,0,0] neg_hi:[1,0,0]
	v_pk_fma_f16 v8, v4, v122, v123 op_sel:[0,1,1] op_sel_hi:[1,1,1] neg_lo:[1,0,0] neg_hi:[1,0,0]
	v_pk_fma_f16 v9, v5, v122, v123 op_sel:[0,1,1] op_sel_hi:[1,1,1] neg_lo:[1,0,0] neg_hi:[1,0,0]
	v_mfma_f32_16x16x32_f16 v[22:25], v[14:17], v[2:5], 0
	ds_read2_b64 v[76:79], v32 offset0:23 offset1:225
	s_waitcnt lgkmcnt(13)
	v_pk_fma_f16 v2, v52, v6, v2
	v_pk_fma_f16 v3, v53, v7, v3
	v_pk_fma_f16 v4, v54, v8, v4
	v_pk_fma_f16 v5, v55, v9, v5
	v_cndmask_b32_e64 v26, v26, v18, s[60:61]
	v_pk_fma_f16 v6, v2, v124, v125 op_sel:[0,1,1] op_sel_hi:[1,1,1] neg_lo:[1,0,0] neg_hi:[1,0,0]
	v_pk_fma_f16 v7, v3, v124, v125 op_sel:[0,1,1] op_sel_hi:[1,1,1] neg_lo:[1,0,0] neg_hi:[1,0,0]
	v_pk_fma_f16 v8, v4, v124, v125 op_sel:[0,1,1] op_sel_hi:[1,1,1] neg_lo:[1,0,0] neg_hi:[1,0,0]
	v_pk_fma_f16 v9, v5, v124, v125 op_sel:[0,1,1] op_sel_hi:[1,1,1] neg_lo:[1,0,0] neg_hi:[1,0,0]
	v_mfma_f32_16x16x32_f16 v[18:21], v[14:17], v[2:5], 0
	ds_read2_b64 v[80:83], v32 offset0:24 offset1:226
	ds_read_b128 v[136:139], v33 offset:192
	v_pk_fma_f16 v2, v56, v6, v2
	v_pk_fma_f16 v3, v57, v7, v3
	v_pk_fma_f16 v4, v58, v8, v4
	v_pk_fma_f16 v5, v59, v9, v5
	v_cndmask_b32_e64 v27, v27, v23, s[60:61]
	v_pk_fma_f16 v6, v2, v126, v127 op_sel:[0,1,1] op_sel_hi:[1,1,1] neg_lo:[1,0,0] neg_hi:[1,0,0]
	v_pk_fma_f16 v7, v3, v126, v127 op_sel:[0,1,1] op_sel_hi:[1,1,1] neg_lo:[1,0,0] neg_hi:[1,0,0]
	v_pk_fma_f16 v8, v4, v126, v127 op_sel:[0,1,1] op_sel_hi:[1,1,1] neg_lo:[1,0,0] neg_hi:[1,0,0]
	v_pk_fma_f16 v9, v5, v126, v127 op_sel:[0,1,1] op_sel_hi:[1,1,1] neg_lo:[1,0,0] neg_hi:[1,0,0]
	v_mfma_f32_16x16x32_f16 v[22:25], v[14:17], v[2:5], 0
	ds_read2_b64 v[84:87], v32 offset0:25 offset1:227
	s_waitcnt lgkmcnt(13)
	v_pk_fma_f16 v2, v60, v6, v2
	v_pk_fma_f16 v3, v61, v7, v3
	v_pk_fma_f16 v4, v62, v8, v4
	v_pk_fma_f16 v5, v63, v9, v5
	v_cndmask_b32_e64 v28, v28, v20, s[60:61]
	v_pk_fma_f16 v6, v2, v128, v129 op_sel:[0,1,1] op_sel_hi:[1,1,1] neg_lo:[1,0,0] neg_hi:[1,0,0]
	v_pk_fma_f16 v7, v3, v128, v129 op_sel:[0,1,1] op_sel_hi:[1,1,1] neg_lo:[1,0,0] neg_hi:[1,0,0]
	v_pk_fma_f16 v8, v4, v128, v129 op_sel:[0,1,1] op_sel_hi:[1,1,1] neg_lo:[1,0,0] neg_hi:[1,0,0]
	v_pk_fma_f16 v9, v5, v128, v129 op_sel:[0,1,1] op_sel_hi:[1,1,1] neg_lo:[1,0,0] neg_hi:[1,0,0]
	v_mfma_f32_16x16x32_f16 v[18:21], v[14:17], v[2:5], 0
	ds_read2_b64 v[88:91], v32 offset0:26 offset1:228
	ds_read_b128 v[140:143], v33 offset:208
	v_pk_fma_f16 v2, v64, v6, v2
	v_pk_fma_f16 v3, v65, v7, v3
	v_pk_fma_f16 v4, v66, v8, v4
	v_pk_fma_f16 v5, v67, v9, v5
	v_cndmask_b32_e64 v29, v29, v25, s[60:61]
	v_pk_fma_f16 v6, v2, v130, v131 op_sel:[0,1,1] op_sel_hi:[1,1,1] neg_lo:[1,0,0] neg_hi:[1,0,0]
	v_pk_fma_f16 v7, v3, v130, v131 op_sel:[0,1,1] op_sel_hi:[1,1,1] neg_lo:[1,0,0] neg_hi:[1,0,0]
	v_pk_fma_f16 v8, v4, v130, v131 op_sel:[0,1,1] op_sel_hi:[1,1,1] neg_lo:[1,0,0] neg_hi:[1,0,0]
	v_pk_fma_f16 v9, v5, v130, v131 op_sel:[0,1,1] op_sel_hi:[1,1,1] neg_lo:[1,0,0] neg_hi:[1,0,0]
	v_mfma_f32_16x16x32_f16 v[22:25], v[14:17], v[2:5], 0
	ds_read2_b64 v[92:95], v32 offset0:27 offset1:229
	s_waitcnt lgkmcnt(6)
	v_pk_fma_f16 v2, v68, v6, v2
	v_pk_fma_f16 v3, v69, v7, v3
	v_pk_fma_f16 v4, v70, v8, v4
	v_pk_fma_f16 v5, v71, v9, v5
	v_cndmask_b32_e64 v26, v26, v18, s[62:63]
	v_pk_fma_f16 v6, v2, v132, v133 op_sel:[0,1,1] op_sel_hi:[1,1,1] neg_lo:[1,0,0] neg_hi:[1,0,0]
	v_pk_fma_f16 v7, v3, v132, v133 op_sel:[0,1,1] op_sel_hi:[1,1,1] neg_lo:[1,0,0] neg_hi:[1,0,0]
	v_pk_fma_f16 v8, v4, v132, v133 op_sel:[0,1,1] op_sel_hi:[1,1,1] neg_lo:[1,0,0] neg_hi:[1,0,0]
	v_pk_fma_f16 v9, v5, v132, v133 op_sel:[0,1,1] op_sel_hi:[1,1,1] neg_lo:[1,0,0] neg_hi:[1,0,0]
	v_mfma_f32_16x16x32_f16 v[18:21], v[14:17], v[2:5], 0
	ds_read2_b64 v[96:99], v32 offset0:28 offset1:230
	ds_read_b128 v[144:147], v33 offset:224
	v_pk_fma_f16 v2, v72, v6, v2
	v_pk_fma_f16 v3, v73, v7, v3
	v_pk_fma_f16 v4, v74, v8, v4
	v_pk_fma_f16 v5, v75, v9, v5
	v_cndmask_b32_e64 v27, v27, v23, s[62:63]
	v_pk_fma_f16 v6, v2, v134, v135 op_sel:[0,1,1] op_sel_hi:[1,1,1] neg_lo:[1,0,0] neg_hi:[1,0,0]
	v_pk_fma_f16 v7, v3, v134, v135 op_sel:[0,1,1] op_sel_hi:[1,1,1] neg_lo:[1,0,0] neg_hi:[1,0,0]
	v_pk_fma_f16 v8, v4, v134, v135 op_sel:[0,1,1] op_sel_hi:[1,1,1] neg_lo:[1,0,0] neg_hi:[1,0,0]
	v_pk_fma_f16 v9, v5, v134, v135 op_sel:[0,1,1] op_sel_hi:[1,1,1] neg_lo:[1,0,0] neg_hi:[1,0,0]
	v_mfma_f32_16x16x32_f16 v[22:25], v[14:17], v[2:5], 0
	ds_read2_b64 v[100:103], v32 offset0:29 offset1:231
	s_waitcnt lgkmcnt(6)
	v_pk_fma_f16 v2, v76, v6, v2
	v_pk_fma_f16 v3, v77, v7, v3
	v_pk_fma_f16 v4, v78, v8, v4
	v_pk_fma_f16 v5, v79, v9, v5
	v_cndmask_b32_e64 v28, v28, v20, s[62:63]
	v_pk_fma_f16 v6, v2, v136, v137 op_sel:[0,1,1] op_sel_hi:[1,1,1] neg_lo:[1,0,0] neg_hi:[1,0,0]
	v_pk_fma_f16 v7, v3, v136, v137 op_sel:[0,1,1] op_sel_hi:[1,1,1] neg_lo:[1,0,0] neg_hi:[1,0,0]
	v_pk_fma_f16 v8, v4, v136, v137 op_sel:[0,1,1] op_sel_hi:[1,1,1] neg_lo:[1,0,0] neg_hi:[1,0,0]
	v_pk_fma_f16 v9, v5, v136, v137 op_sel:[0,1,1] op_sel_hi:[1,1,1] neg_lo:[1,0,0] neg_hi:[1,0,0]
	v_mfma_f32_16x16x32_f16 v[18:21], v[14:17], v[2:5], 0
	ds_read2_b64 v[104:107], v32 offset0:30 offset1:232
	ds_read_b128 v[148:151], v33 offset:240
	v_pk_fma_f16 v2, v80, v6, v2
	v_pk_fma_f16 v3, v81, v7, v3
	v_pk_fma_f16 v4, v82, v8, v4
	v_pk_fma_f16 v5, v83, v9, v5
	v_cndmask_b32_e64 v29, v29, v25, s[62:63]
	v_readfirstlane_b32 s4, v37
	v_readfirstlane_b32 s5, v38
	s_and_b32 s4, s4, s5
	s_cbranch_scc0 .Lc1_slow1

.Lc1_nd1:
	v_pk_fma_f16 v6, v2, v138, v139 op_sel:[0,1,1] op_sel_hi:[1,1,1] neg_lo:[1,0,0] neg_hi:[1,0,0]
	v_pk_fma_f16 v7, v3, v138, v139 op_sel:[0,1,1] op_sel_hi:[1,1,1] neg_lo:[1,0,0] neg_hi:[1,0,0]
	v_pk_fma_f16 v8, v4, v138, v139 op_sel:[0,1,1] op_sel_hi:[1,1,1] neg_lo:[1,0,0] neg_hi:[1,0,0]
	v_pk_fma_f16 v9, v5, v138, v139 op_sel:[0,1,1] op_sel_hi:[1,1,1] neg_lo:[1,0,0] neg_hi:[1,0,0]
	v_mfma_f32_16x16x32_f16 v[22:25], v[14:17], v[2:5], 0
	ds_read2_b64 v[108:111], v32 offset0:31 offset1:233
	s_waitcnt lgkmcnt(6)
	v_pk_fma_f16 v2, v84, v6, v2
	v_pk_fma_f16 v3, v85, v7, v3
	v_pk_fma_f16 v4, v86, v8, v4
	v_pk_fma_f16 v5, v87, v9, v5
	v_cndmask_b32_e64 v26, v26, v18, s[64:65]
	v_pk_fma_f16 v6, v2, v140, v141 op_sel:[0,1,1] op_sel_hi:[1,1,1] neg_lo:[1,0,0] neg_hi:[1,0,0]
	v_pk_fma_f16 v7, v3, v140, v141 op_sel:[0,1,1] op_sel_hi:[1,1,1] neg_lo:[1,0,0] neg_hi:[1,0,0]
	v_pk_fma_f16 v8, v4, v140, v141 op_sel:[0,1,1] op_sel_hi:[1,1,1] neg_lo:[1,0,0] neg_hi:[1,0,0]
	v_pk_fma_f16 v9, v5, v140, v141 op_sel:[0,1,1] op_sel_hi:[1,1,1] neg_lo:[1,0,0] neg_hi:[1,0,0]
	v_mfma_f32_16x16x32_f16 v[18:21], v[14:17], v[2:5], 0
	ds_read2_b64 v[48:51], v32 offset0:32 offset1:234
	ds_read_b128 v[120:123], v33 offset:256
	ds_read2_b64 v[10:13], v34 offset0:32 offset1:234
	v_pk_fma_f16 v2, v88, v6, v2
	v_pk_fma_f16 v3, v89, v7, v3
	v_pk_fma_f16 v4, v90, v8, v4
	v_pk_fma_f16 v5, v91, v9, v5
	v_cndmask_b32_e64 v27, v27, v23, s[64:65]
	v_pk_fma_f16 v6, v2, v142, v143 op_sel:[0,1,1] op_sel_hi:[1,1,1] neg_lo:[1,0,0] neg_hi:[1,0,0]
	v_pk_fma_f16 v7, v3, v142, v143 op_sel:[0,1,1] op_sel_hi:[1,1,1] neg_lo:[1,0,0] neg_hi:[1,0,0]
	v_pk_fma_f16 v8, v4, v142, v143 op_sel:[0,1,1] op_sel_hi:[1,1,1] neg_lo:[1,0,0] neg_hi:[1,0,0]
	v_pk_fma_f16 v9, v5, v142, v143 op_sel:[0,1,1] op_sel_hi:[1,1,1] neg_lo:[1,0,0] neg_hi:[1,0,0]
	v_mfma_f32_16x16x32_f16 v[22:25], v[14:17], v[2:5], 0
	ds_read2_b64 v[52:55], v32 offset0:33 offset1:235
	s_waitcnt lgkmcnt(7)
	v_pk_fma_f16 v2, v92, v6, v2
	v_pk_fma_f16 v3, v93, v7, v3
	v_pk_fma_f16 v4, v94, v8, v4
	v_pk_fma_f16 v5, v95, v9, v5
	v_cndmask_b32_e64 v28, v28, v20, s[64:65]
	v_pk_fma_f16 v6, v2, v144, v145 op_sel:[0,1,1] op_sel_hi:[1,1,1] neg_lo:[1,0,0] neg_hi:[1,0,0]
	v_pk_fma_f16 v7, v3, v144, v145 op_sel:[0,1,1] op_sel_hi:[1,1,1] neg_lo:[1,0,0] neg_hi:[1,0,0]
	v_pk_fma_f16 v8, v4, v144, v145 op_sel:[0,1,1] op_sel_hi:[1,1,1] neg_lo:[1,0,0] neg_hi:[1,0,0]
	v_pk_fma_f16 v9, v5, v144, v145 op_sel:[0,1,1] op_sel_hi:[1,1,1] neg_lo:[1,0,0] neg_hi:[1,0,0]
	v_mfma_f32_16x16x32_f16 v[18:21], v[14:17], v[2:5], 0
	ds_read2_b64 v[56:59], v32 offset0:34 offset1:236
	ds_read_b128 v[124:127], v33 offset:272
	v_pk_fma_f16 v2, v96, v6, v2
	v_pk_fma_f16 v3, v97, v7, v3
	v_pk_fma_f16 v4, v98, v8, v4
	v_pk_fma_f16 v5, v99, v9, v5
	v_cndmask_b32_e64 v29, v29, v25, s[64:65]
	s_cmp_eq_u32 s72, 1
	s_cbranch_scc0 .Lc1_ns1
	s_waitcnt lgkmcnt(7)
	v_readfirstlane_b32 s4, v45
	s_cmp_eq_u32 s4, 4
	s_cbranch_scc0 .Lc1_dslow1

.Lc1_ns1:
	v_pk_fma_f16 v6, v2, v146, v147 op_sel:[0,1,1] op_sel_hi:[1,1,1] neg_lo:[1,0,0] neg_hi:[1,0,0]
	v_pk_fma_f16 v7, v3, v146, v147 op_sel:[0,1,1] op_sel_hi:[1,1,1] neg_lo:[1,0,0] neg_hi:[1,0,0]
	v_pk_fma_f16 v8, v4, v146, v147 op_sel:[0,1,1] op_sel_hi:[1,1,1] neg_lo:[1,0,0] neg_hi:[1,0,0]
	v_pk_fma_f16 v9, v5, v146, v147 op_sel:[0,1,1] op_sel_hi:[1,1,1] neg_lo:[1,0,0] neg_hi:[1,0,0]
	v_mfma_f32_16x16x32_f16 v[22:25], v[14:17], v[2:5], 0
	ds_read2_b64 v[60:63], v32 offset0:35 offset1:237
	s_waitcnt lgkmcnt(7)
	v_pk_fma_f16 v2, v100, v6, v2
	v_pk_fma_f16 v3, v101, v7, v3
	v_pk_fma_f16 v4, v102, v8, v4
	v_pk_fma_f16 v5, v103, v9, v5
	v_cndmask_b32_e64 v26, v26, v18, s[66:67]
	v_pk_fma_f16 v6, v2, v148, v149 op_sel:[0,1,1] op_sel_hi:[1,1,1] neg_lo:[1,0,0] neg_hi:[1,0,0]
	v_pk_fma_f16 v7, v3, v148, v149 op_sel:[0,1,1] op_sel_hi:[1,1,1] neg_lo:[1,0,0] neg_hi:[1,0,0]
	v_pk_fma_f16 v8, v4, v148, v149 op_sel:[0,1,1] op_sel_hi:[1,1,1] neg_lo:[1,0,0] neg_hi:[1,0,0]
	v_pk_fma_f16 v9, v5, v148, v149 op_sel:[0,1,1] op_sel_hi:[1,1,1] neg_lo:[1,0,0] neg_hi:[1,0,0]
	v_mfma_f32_16x16x32_f16 v[18:21], v[14:17], v[2:5], 0
	ds_read2_b64 v[64:67], v32 offset0:36 offset1:238
	ds_read_b128 v[128:131], v33 offset:288
	v_pk_fma_f16 v2, v104, v6, v2
	v_pk_fma_f16 v3, v105, v7, v3
	v_pk_fma_f16 v4, v106, v8, v4
	v_pk_fma_f16 v5, v107, v9, v5
	v_cndmask_b32_e64 v27, v27, v23, s[66:67]
	v_pk_fma_f16 v6, v2, v150, v151 op_sel:[0,1,1] op_sel_hi:[1,1,1] neg_lo:[1,0,0] neg_hi:[1,0,0]
	v_pk_fma_f16 v7, v3, v150, v151 op_sel:[0,1,1] op_sel_hi:[1,1,1] neg_lo:[1,0,0] neg_hi:[1,0,0]
	v_pk_fma_f16 v8, v4, v150, v151 op_sel:[0,1,1] op_sel_hi:[1,1,1] neg_lo:[1,0,0] neg_hi:[1,0,0]
	v_pk_fma_f16 v9, v5, v150, v151 op_sel:[0,1,1] op_sel_hi:[1,1,1] neg_lo:[1,0,0] neg_hi:[1,0,0]
	v_mfma_f32_16x16x32_f16 v[22:25], v[14:17], v[2:5], 0
	ds_read2_b64 v[68:71], v32 offset0:37 offset1:239
	s_waitcnt lgkmcnt(6)
	v_pk_fma_f16 v2, v108, v6, v2
	v_pk_fma_f16 v3, v109, v7, v3
	v_pk_fma_f16 v4, v110, v8, v4
	v_pk_fma_f16 v5, v111, v9, v5
	v_cndmask_b32_e64 v28, v28, v20, s[66:67]
.Lc1_next1:
	v_add_u32_e32 v32, 0x100, v32
	v_add_u32_e32 v33, 0x100, v33
	v_add_u32_e32 v34, 0x100, v34
	v_add_u32_e32 v36, 8, v36
	v_add_u32_e32 v39, 0x1000, v39
	v_add_u32_e32 v43, 0x1000, v43
	v_add_u32_e32 v35, 0x800, v35
	s_xor_b32 s71, s71, 2
	s_add_i32 s70, s70, 1
	s_cmp_lt_u32 s70, 6
	s_cbranch_scc1 .Lc1_loop
	v_pk_fma_f16 v6, v2, v120, v121 op_sel:[0,1,1] op_sel_hi:[1,1,1] neg_lo:[1,0,0] neg_hi:[1,0,0]
	v_pk_fma_f16 v7, v3, v120, v121 op_sel:[0,1,1] op_sel_hi:[1,1,1] neg_lo:[1,0,0] neg_hi:[1,0,0]
	v_pk_fma_f16 v8, v4, v120, v121 op_sel:[0,1,1] op_sel_hi:[1,1,1] neg_lo:[1,0,0] neg_hi:[1,0,0]
	v_pk_fma_f16 v9, v5, v120, v121 op_sel:[0,1,1] op_sel_hi:[1,1,1] neg_lo:[1,0,0] neg_hi:[1,0,0]
	v_mfma_f32_16x16x32_f16 v[18:21], v[10:13], v[2:5], 0
	ds_read2_b64 v[72:75], v32 offset0:6 offset1:208
	ds_read_b128 v[132:135], v33 offset:48
	v_pk_fma_f16 v2, v48, v6, v2
	v_pk_fma_f16 v3, v49, v7, v3
	v_pk_fma_f16 v4, v50, v8, v4
	v_pk_fma_f16 v5, v51, v9, v5
	v_cndmask_b32_e64 v29, v29, v25, s[66:67]
	v_cvt_pk_f16_f32 v30, v26, v27
	v_cvt_pk_f16_f32 v31, v28, v29
	ds_write_b16 v39, v30 offset:0
	ds_write_b16_d16_hi v39, v30 offset:64
	ds_write_b16 v39, v31 offset:128
	ds_write_b16_d16_hi v39, v31 offset:192
	s_mov_b64 exec, 1
	ds_add_u32 v36, v44 offset:124
	s_mov_b64 exec, -1
	v_pk_fma_f16 v6, v2, v122, v123 op_sel:[0,1,1] op_sel_hi:[1,1,1] neg_lo:[1,0,0] neg_hi:[1,0,0]
	v_pk_fma_f16 v7, v3, v122, v123 op_sel:[0,1,1] op_sel_hi:[1,1,1] neg_lo:[1,0,0] neg_hi:[1,0,0]
	v_pk_fma_f16 v8, v4, v122, v123 op_sel:[0,1,1] op_sel_hi:[1,1,1] neg_lo:[1,0,0] neg_hi:[1,0,0]
	v_pk_fma_f16 v9, v5, v122, v123 op_sel:[0,1,1] op_sel_hi:[1,1,1] neg_lo:[1,0,0] neg_hi:[1,0,0]
	v_mfma_f32_16x16x32_f16 v[22:25], v[10:13], v[2:5], 0
	ds_read2_b64 v[76:79], v32 offset0:7 offset1:209
	s_waitcnt lgkmcnt(11)
	v_pk_fma_f16 v2, v52, v6, v2
	v_pk_fma_f16 v3, v53, v7, v3
	v_pk_fma_f16 v4, v54, v8, v4
	v_pk_fma_f16 v5, v55, v9, v5
	v_cndmask_b32_e64 v26, v26, v18, s[60:61]
	v_pk_fma_f16 v6, v2, v124, v125 op_sel:[0,1,1] op_sel_hi:[1,1,1] neg_lo:[1,0,0] neg_hi:[1,0,0]
	v_pk_fma_f16 v7, v3, v124, v125 op_sel:[0,1,1] op_sel_hi:[1,1,1] neg_lo:[1,0,0] neg_hi:[1,0,0]
	v_pk_fma_f16 v8, v4, v124, v125 op_sel:[0,1,1] op_sel_hi:[1,1,1] neg_lo:[1,0,0] neg_hi:[1,0,0]
	v_pk_fma_f16 v9, v5, v124, v125 op_sel:[0,1,1] op_sel_hi:[1,1,1] neg_lo:[1,0,0] neg_hi:[1,0,0]
	v_mfma_f32_16x16x32_f16 v[18:21], v[10:13], v[2:5], 0
	v_pk_fma_f16 v2, v56, v6, v2
	v_pk_fma_f16 v3, v57, v7, v3
	v_pk_fma_f16 v4, v58, v8, v4
	v_pk_fma_f16 v5, v59, v9, v5
	v_cndmask_b32_e64 v27, v27, v23, s[60:61]
	v_pk_fma_f16 v6, v2, v126, v127 op_sel:[0,1,1] op_sel_hi:[1,1,1] neg_lo:[1,0,0] neg_hi:[1,0,0]
	v_pk_fma_f16 v7, v3, v126, v127 op_sel:[0,1,1] op_sel_hi:[1,1,1] neg_lo:[1,0,0] neg_hi:[1,0,0]
	v_pk_fma_f16 v8, v4, v126, v127 op_sel:[0,1,1] op_sel_hi:[1,1,1] neg_lo:[1,0,0] neg_hi:[1,0,0]
	v_pk_fma_f16 v9, v5, v126, v127 op_sel:[0,1,1] op_sel_hi:[1,1,1] neg_lo:[1,0,0] neg_hi:[1,0,0]
	v_mfma_f32_16x16x32_f16 v[22:25], v[10:13], v[2:5], 0
	s_waitcnt lgkmcnt(8)
	v_pk_fma_f16 v2, v60, v6, v2
	v_pk_fma_f16 v3, v61, v7, v3
	v_pk_fma_f16 v4, v62, v8, v4
	v_pk_fma_f16 v5, v63, v9, v5
	v_cndmask_b32_e64 v28, v28, v20, s[60:61]
	s_mov_b32 s72, 0
	s_cmp_eq_u32 s70, 0
	s_cbranch_scc1 .Lc1_ndt
	s_cmp_eq_u32 s36, 3
	s_cbranch_scc0 .Lc1_ndt
	s_mov_b32 s72, 1
	ds_read_b32 v45, v36 offset:124
	ds_read_b128 v[112:115], v43 offset:0
	ds_read_b128 v[116:119], v43 offset:1024
.Lc1_ndt:
	v_pk_fma_f16 v6, v2, v128, v129 op_sel:[0,1,1] op_sel_hi:[1,1,1] neg_lo:[1,0,0] neg_hi:[1,0,0]
	v_pk_fma_f16 v7, v3, v128, v129 op_sel:[0,1,1] op_sel_hi:[1,1,1] neg_lo:[1,0,0] neg_hi:[1,0,0]
	v_pk_fma_f16 v8, v4, v128, v129 op_sel:[0,1,1] op_sel_hi:[1,1,1] neg_lo:[1,0,0] neg_hi:[1,0,0]
	v_pk_fma_f16 v9, v5, v128, v129 op_sel:[0,1,1] op_sel_hi:[1,1,1] neg_lo:[1,0,0] neg_hi:[1,0,0]
	v_mfma_f32_16x16x32_f16 v[18:21], v[10:13], v[2:5], 0
	v_pk_fma_f16 v2, v64, v6, v2
	v_pk_fma_f16 v3, v65, v7, v3
	v_pk_fma_f16 v4, v66, v8, v4
	v_pk_fma_f16 v5, v67, v9, v5
	v_cndmask_b32_e64 v29, v29, v25, s[60:61]
	v_pk_fma_f16 v6, v2, v130, v131 op_sel:[0,1,1] op_sel_hi:[1,1,1] neg_lo:[1,0,0] neg_hi:[1,0,0]
	v_pk_fma_f16 v7, v3, v130, v131 op_sel:[0,1,1] op_sel_hi:[1,1,1] neg_lo:[1,0,0] neg_hi:[1,0,0]
	v_pk_fma_f16 v8, v4, v130, v131 op_sel:[0,1,1] op_sel_hi:[1,1,1] neg_lo:[1,0,0] neg_hi:[1,0,0]
	v_pk_fma_f16 v9, v5, v130, v131 op_sel:[0,1,1] op_sel_hi:[1,1,1] neg_lo:[1,0,0] neg_hi:[1,0,0]
	v_mfma_f32_16x16x32_f16 v[22:25], v[10:13], v[2:5], 0
	s_waitcnt lgkmcnt(0)
	v_pk_fma_f16 v2, v68, v6, v2
	v_pk_fma_f16 v3, v69, v7, v3
	v_pk_fma_f16 v4, v70, v8, v4
	v_pk_fma_f16 v5, v71, v9, v5
	v_cndmask_b32_e64 v26, v26, v18, s[62:63]
	v_pk_fma_f16 v6, v2, v132, v133 op_sel:[0,1,1] op_sel_hi:[1,1,1] neg_lo:[1,0,0] neg_hi:[1,0,0]
	v_pk_fma_f16 v7, v3, v132, v133 op_sel:[0,1,1] op_sel_hi:[1,1,1] neg_lo:[1,0,0] neg_hi:[1,0,0]
	v_pk_fma_f16 v8, v4, v132, v133 op_sel:[0,1,1] op_sel_hi:[1,1,1] neg_lo:[1,0,0] neg_hi:[1,0,0]
	v_pk_fma_f16 v9, v5, v132, v133 op_sel:[0,1,1] op_sel_hi:[1,1,1] neg_lo:[1,0,0] neg_hi:[1,0,0]
	v_mfma_f32_16x16x32_f16 v[18:21], v[10:13], v[2:5], 0
	v_pk_fma_f16 v2, v72, v6, v2
	v_pk_fma_f16 v3, v73, v7, v3
	v_pk_fma_f16 v4, v74, v8, v4
	v_pk_fma_f16 v5, v75, v9, v5
	v_cndmask_b32_e64 v27, v27, v23, s[62:63]
	s_cmp_eq_u32 s72, 1
	s_cbranch_scc0 .Lc1_nst
	s_waitcnt lgkmcnt(0)
	v_readfirstlane_b32 s4, v45
	s_cmp_eq_u32 s4, 4
	s_cbranch_scc0 .Lc1_dslowt
